# batched Q-row loads in all four attention unit prologues (were 8 serialized load/wait/ds_write each) on top of batched tile-table + Wo residual loads
# speedup vs baseline: 1.0063x; 1.0063x over previous
; __device__ __forceinline__ unsigned ld_sc1(const unsigned* p) { return __hip_atomic_load(p, __ATOMIC_RELAXED, __HIP_MEMORY_SCOPE_AGENT); }
; template <int mode> __device__ __forceinline__ void attn_unit(const AttnArgs& A, const int b, const int h, const int sub, char* shm, const int wave_) {
;     ...
;     if (mode == 3) { gk = sub >> 4; const int c = sub & 15; const int li = (b * 5 + (h - 6)) * 15 + gk;
;         gcnt = __builtin_amdgcn_readfirstlane((int)ld_sc1(A.mcnt + li));
;         if (c * 256 >= gcnt) return;
;         const int gi = c * 256 + wid * 32 + r32; gvalid = gi < gcnt; wvalid = (c * 256 + wid * 32) < gcnt;
;         gent = ld_sc1(A.mlist + (size_t)li * MLCAP + (gvalid ? gi : 0)); qb = 0; }
;     const size_t rowbase = (size_t)b * SEQ + res; const int q0 = qb * 256;
;     const bf16* Qp = A.qkv + (rowbase + (size_t)dil * ((mode == 3) ? (int)(gent & 4095u) : (q0 + wid * 32 + r32))) * QS + h * 128;
;     const bf16* Kh = A.qkv + rowbase * QS + 2048 + h * 128;
;     const bf16* Vh = A.qkv + rowbase * QS + 4096 + h * 128;
;     const size_t rstep = (size_t)dil * QS;
;     char* V_lds = shm + L_V; char* K_lds = shm + L_K;
;     float* wsf = (float*)(shm + L_WS) + wid * 64; float* li_l = wsf; float* al_l = wsf + 32;
;     int* TL = (int*)(shm + L_TL); int* FLG = (int*)(shm + L_FLG); unsigned* MSK = (unsigned*)(shm + L_MSK); float* KM = (float*)(shm + L_KM);
;     char* qf = shm + L_Q + wid * 8192 + lane * 16;
;     const int qw0 = q0 + wid * 32;
;     const int pos = qw0 + r32;
;     const int vb0 = (int)(uintptr_t)V_lds + v_rd_base(lane);
;     unsigned koffb[2], voffb[2];
; #pragma unroll
;     for (int i = 0; i < 2; ++i) { const int Lb = (2 * wid + i) * 1024 + lane * 16;
;         const int rowk = Lb >> 8, ck = ((Lb >> 4) & 15) ^ (rowk & 7);
;         koffb[i] = (unsigned)(((size_t)rowk * rstep + ck * 8) * 2);
;         const int sub_ = Lb >> 9, win_ = Lb & 511, kk = (sub_ >> 2) * 8 + (win_ >> 6), kv = (kk & ~0xC) | ((kk & 4) << 1) | ((kk & 8) >> 1), cc = (sub_ & 3) * 4 + ((win_ & 63) >> 4);
;         voffb[i] = (unsigned)(((size_t)kv * rstep + cc * 8) * 2); }
;     typedef __attribute__((address_space(3))) unsigned lds_u32;
;     lds_u32* const Kdst = (lds_u32*)(K_lds + wid * 2048); lds_u32* const Vdst = (lds_u32*)(V_lds + wid * 2048);
;     ...
;     { const int kf_ = ((mode == 3) ? gk * 256 : q0) + 192; TDMA(kf_, 0); }
;     bf16x8 qr[8];
; #pragma unroll
.LBB0_516:
	s_bfe_u32 s1, s26, 0x1000b
	s_bfe_u32 s19, s26, 0x30008
	s_mul_i32 s14, s1, 5
	s_add_i32 s14, s14, s19
	s_bfe_u32 s0, s26, 0x40004
	s_mul_i32 s14, s14, 15
	s_add_i32 s14, s14, s0
	v_mbcnt_lo_u32_b32 v0, -1, 0
	v_mbcnt_hi_u32_b32 v0, -1, v0
	s_lshl_b32 s15, s14, 2
	v_readlane_b32 s16, v255, 10
	s_waitcnt vmcnt(18)
	v_add_u32_e32 v119, s94, v0
	v_mov_b32_e32 v0, s15
	v_readlane_b32 s17, v255, 11
	s_lshl_b32 s15, s26, 8
	s_and_b32 s25, s15, 0xf00
	s_nop 2
	global_load_dword v0, v0, s[16:17] sc1
	s_waitcnt vmcnt(0)
	v_readfirstlane_b32 s24, v0
	s_cmp_ge_i32 s25, s24
	s_cbranch_scc1 .LBB0_666
	v_readlane_b32 s15, v252, 37
	v_and_b32_e32 v120, 31, v119
	s_add_i32 s25, s25, s15
	s_add_i32 s22, s19, 6
	v_or_b32_e32 v0, s25, v120
	s_mulk_i32 s14, 0x3c00
	v_readlane_b32 s16, v255, 8
	v_cmp_gt_i32_e64 s[40:41], s24, v0
	v_readlane_b32 s17, v255, 9
	s_add_u32 s14, s16, s14
	s_addc_u32 s15, s17, 0
	v_cndmask_b32_e64 v0, 0, v0, s[40:41]
	v_lshl_add_u64 v[2:3], v[0:1], 2, s[14:15]
	global_load_dword v122, v[2:3], off sc1
	s_lshl_b32 s14, s1, 12
	s_lshl_b32 s18, s22, 7
	s_mul_i32 s1, s1, 0x3000000
	s_add_u32 s1, s38, s1
	s_addc_u32 s15, s39, 0
	s_lshl_b32 s30, s22, 8
	s_add_u32 s1, s1, s30
	v_and_b32_e32 v4, 63, v119
	s_addc_u32 s27, s15, 0
	v_lshlrev_b32_e32 v6, 4, v4
	v_readlane_b32 s23, v252, 28
	v_lshrrev_b32_e32 v8, 1, v119
	s_add_u32 s15, s1, 0x1000
	v_or_b32_e32 v2, s23, v6
	v_bfe_u32 v7, v119, 2, 2
	v_and_b32_e32 v8, 8, v8
	v_readlane_b32 s23, v252, 13
	s_addc_u32 s22, s27, 0
	v_and_b32_e32 v3, 15, v119
	v_or3_b32 v7, v7, v8, s23
	s_add_u32 s23, s1, 0x2000
	v_ashrrev_i32_e32 v9, 8, v2
	s_addc_u32 s27, s27, 0
	s_lshl_b32 s0, s0, 8
	v_bitop3_b32 v10, v9, v3, 3 bitop3:0x6c
	v_mul_i32_i24_e32 v9, 0x3000, v9
	s_or_b32 s28, s0, 0xc0
	v_and_b32_e32 v8, 3, v119
	v_lshl_or_b32 v125, v10, 4, v9
	v_lshrrev_b32_e32 v9, 3, v119
	s_mul_i32 s29, s28, 0x3000
	v_mul_lo_u32 v7, v7, s70
	v_and_or_b32 v9, v9, 4, v8
	v_or_b32_e32 v2, 0x400, v2
	s_add_u32 s0, s15, s29
	v_lshl_or_b32 v126, v9, 4, v7
	v_ashrrev_i32_e32 v9, 8, v2
	v_lshrrev_b32_e32 v2, 7, v2
	s_addc_u32 s1, s22, 0
	v_bitop3_b32 v3, v9, v3, 7 bitop3:0x6c
	v_mul_i32_i24_e32 v9, 0x3000, v9
	v_and_or_b32 v2, v2, 12, v8
	s_add_u32 s34, s23, s29
	v_bfe_u32 v5, v119, 5, 1
	v_lshl_or_b32 v127, v3, 4, v9
	v_lshl_or_b32 v128, v2, 4, v7
	s_mov_b32 s31, s90
	s_addc_u32 s35, s27, 0
	v_mov_b32_e32 v7, v125
	s_add_i32 m0, s2, 0x8000
	v_lshlrev_b32_e32 v114, 4, v5
	v_mov_b32_e32 v115, v1
	v_cmp_gt_i32_e32 vcc, 4, v119
	s_waitcnt vmcnt(0)
	v_and_b32_e32 v121, 0xfff, v122
	v_or_b32_e32 v0, s14, v121
	v_mul_u32_u24_e32 v0, 0x1800, v0
	v_lshlrev_b32_e32 v0, 1, v0
	v_lshl_add_u64 v[2:3], s[38:39], 0, v[0:1]
	v_mov_b32_e32 v0, v126
	v_lshl_add_u64 v[2:3], v[2:3], 0, s[30:31]
	global_load_lds_dwordx4 v7, s[0:1]
	s_mov_b32 m0, s2
	v_mov_b32_e32 v7, v127
	global_load_lds_dwordx4 v0, s[34:35]
	v_mov_b32_e32 v0, v128
	v_lshl_add_u64 v[2:3], v[2:3], 0, v[114:115]
	global_load_dwordx4 v[8:11], v[2:3], off
	global_load_dwordx4 v[16:19], v[2:3], off offset:32
	global_load_dwordx4 v[20:23], v[2:3], off offset:64
	global_load_dwordx4 v[24:27], v[2:3], off offset:96
	global_load_dwordx4 v[28:31], v[2:3], off offset:128
	global_load_dwordx4 v[32:35], v[2:3], off offset:160
	global_load_dwordx4 v[36:39], v[2:3], off offset:192
	global_load_dwordx4 v[40:43], v[2:3], off offset:224
	s_add_i32 m0, s2, 0x8400
	s_nop 0
	global_load_lds_dwordx4 v7, s[0:1]
	v_readlane_b32 s0, v252, 15
	s_add_i32 m0, s2, 0x400
	s_nop 0
	v_add_u32_e32 v123, s0, v6
	global_load_lds_dwordx4 v0, s[34:35]
	s_waitcnt vmcnt(0)
	ds_write_b128 v123, v[8:11]
	ds_write_b128 v123, v[16:19] offset:1024
	ds_write_b128 v123, v[20:23] offset:2048
	ds_write_b128 v123, v[24:27] offset:3072
	ds_write_b128 v123, v[28:31] offset:4096
	ds_write_b128 v123, v[32:35] offset:5120
	ds_write_b128 v123, v[36:39] offset:6144
	ds_write_b128 v123, v[40:43] offset:7168
	s_and_saveexec_b64 s[0:1], vcc
	v_lshl_add_u32 v0, v119, 2, 0
	v_lshlrev_b32_e32 v2, 6, v119
	v_add_u32_e32 v0, 0x20800, v0
	v_sub_u32_e32 v2, s28, v2
	ds_write_b32 v0, v2
	s_or_b64 exec, exec, s[0:1]
	s_cmp_lt_i32 s25, s24
	s_cselect_b64 s[24:25], -1, 0
	s_lshl_b32 s0, s19, 3
	s_sub_i32 s0, 0xffffffc8, s0
	v_cvt_f32_i32_e32 v0, s0
	s_mov_b32 s28, 0x41300000
	v_lshlrev_b32_e32 v5, 2, v5
	v_and_b32_e32 v22, 0xc0, v6
	v_div_scale_f32 v2, s[0:1], s28, s28, v0
	v_rcp_f32_e32 v3, v2
	v_div_scale_f32 v7, vcc, v0, s28, v0
	v_or_b32_e32 v6, 2, v5
	v_fma_f32 v8, -v2, v3, 1.0
	v_fmac_f32_e32 v3, v8, v3
	v_mul_f32_e32 v8, v7, v3
	v_fma_f32 v9, -v2, v8, v7
	v_fmac_f32_e32 v8, v9, v3
	v_fma_f32 v2, -v2, v8, v7
	v_div_fmas_f32 v2, v2, v3, v8
	v_div_fixup_f32 v0, v2, s28, v0
	v_exp_f32_e32 v0, v0
	v_or_b32_e32 v2, 3, v5
	v_cvt_f32_ubyte0_e32 v3, v2
	v_cvt_f32_ubyte0_e32 v2, v6
	v_mul_f32_e32 v118, 0x3fb8aa3b, v0
	v_lshlrev_b32_e32 v21, 1, v4
	v_or_b32_e32 v0, 1, v5
	v_pk_mul_f32 v[68:69], v[118:119], v[2:3] op_sel_hi:[0,1]
	v_mov_b32_e32 v116, 0xf149f2ca
	v_mov_b32_e32 v117, v1
	v_mov_b32_e32 v2, v1
	v_lshlrev_b32_e32 v20, 3, v4
	v_cvt_f32_ubyte0_e32 v19, v0
	v_and_b32_e32 v0, 32, v21
	s_waitcnt lgkmcnt(0)
	s_barrier
; #define tid (tid_of(wave))
; template <int mode> __device__ __forceinline__ void attn_unit(const AttnArgs& A, const int b, const int h, const int sub, char* shm, const int wave_) {
;     ...
;     const float sl = (mode == 2) ? 0.f : __builtin_amdgcn_exp2f(-8.0f * (float)(h + 1) / 11.0f) * 1.4426950408889634f * (float)dil;
;     f32x16 binit;
; #pragma unroll
;     for (int r = 0; r < 16; ++r) binit[r] = sl * (float)((r & 3) + 8 * (r >> 2) + 4 * hi);
;     const float sl32 = 32.f * sl;
;     int NT = 0;
;     if (mode == 1) { NT = 4; if (tid < 4) TL[tid] = q0 + 192 - 64 * tid; }
;     else if (mode == 3) { NT = 4; if (tid < 4) TL[tid] = gk * 256 + 192 - 64 * tid; }
;     else if (mode == 0) {
;         const int lo = q0 >= 128 ? q0 - 128 : 0; NT = (q0 + 256 - lo) / 64;
;         if (tid < NT) TL[NT - 1 - tid] = lo + 64 * tid;
;     } else {
;         NT = (q0 + 256) / 64;
;         if (tid < NT) TL[tid] = q0 + 192 - 64 * tid;
;     }
;     __syncthreads();
;     float m_reg = -1e30f, l_reg = 0.f, carry = 0.f; asm volatile("" : "+v"(m_reg), "+v"(l_reg), "+v"(carry));
;     f32x16 o[4];
; #pragma unroll
;     for (int d0 = 0; d0 < 4; ++d0) o[d0] = f32x16{};
;     bool wdone = false;
	s_movk_i32 s0, 0x118
	v_or_b32_e32 v8, 8, v5
	v_or_b32_e32 v10, 10, v5
	v_or_b32_e32 v12, 16, v5
	v_or_b32_e32 v14, 18, v5
	v_or_b32_e32 v15, 25, v5
	v_or_b32_e32 v16, 24, v5
	v_and_or_b32 v0, v20, s0, v0
	v_lshlrev_b32_e32 v2, 4, v120
	s_movk_i32 s0, 0x70
	v_or_b32_e32 v7, 9, v5
	v_or_b32_e32 v9, 11, v5
	v_or_b32_e32 v11, 17, v5
	v_or_b32_e32 v13, 19, v5
	v_or_b32_e32 v18, 26, v5
	v_cvt_f32_ubyte0_e32 v6, v8
	v_cvt_f32_ubyte0_e32 v8, v10
	v_cvt_f32_ubyte0_e32 v10, v12
	v_cvt_f32_ubyte0_e32 v12, v14
	v_cvt_f32_ubyte0_e32 v15, v15
	v_cvt_f32_ubyte0_e32 v14, v16
	v_and_b32_e32 v3, 0x70, v2
	v_bitop3_b32 v135, v114, v2, s0 bitop3:0x78
	s_movk_i32 s0, 0x60
	s_cmp_lg_u32 0, -1
	v_or_b32_e32 v17, 27, v5
	v_cvt_f32_ubyte0_e32 v7, v7
	v_cvt_f32_ubyte0_e32 v9, v9
	v_cvt_f32_ubyte0_e32 v11, v11
	v_cvt_f32_ubyte0_e32 v13, v13
	v_cvt_f32_ubyte0_e32 v16, v18
	v_cvt_f32_ubyte0_e32 v18, v5
	v_pk_mul_f32 v[78:79], v[118:119], v[14:15] op_sel_hi:[0,1]
	v_bitop3_b32 v131, v114, v3, s0 bitop3:0x36
	s_cselect_b32 s0, 0, 0
	v_mov_b32_e32 v14, v1
	v_mov_b32_e32 v15, v1
	v_cvt_f32_ubyte0_e32 v17, v17
	v_pk_mul_f32 v[76:77], v[118:119], v[12:13] op_sel_hi:[0,1]
	v_pk_mul_f32 v[74:75], v[118:119], v[10:11] op_sel_hi:[0,1]
	v_pk_mul_f32 v[72:73], v[118:119], v[8:9] op_sel_hi:[0,1]
	v_pk_mul_f32 v[70:71], v[118:119], v[6:7] op_sel_hi:[0,1]
	v_pk_mul_f32 v[66:67], v[118:119], v[18:19] op_sel_hi:[0,1]
	v_bitop3_b32 v134, v114, v3, 32 bitop3:0x36
	v_bitop3_b32 v132, v114, v3, 64 bitop3:0x36
	v_cmp_gt_u32_e64 s[42:43], 32, v4
	v_add3_u32 v124, v22, s0, v0
	v_mov_b32_e32 v0, v1
	v_mov_b32_e32 v2, v1
	v_mov_b32_e32 v3, v1
	v_mov_b32_e32 v4, v1
	v_mov_b32_e32 v5, v1
	v_mov_b32_e32 v6, v1
	v_mov_b32_e32 v7, v1
	v_mov_b32_e32 v8, v1
	v_mov_b32_e32 v9, v1
	v_mov_b32_e32 v10, v1
	v_mov_b32_e32 v11, v1
	v_mov_b32_e32 v12, v1
	v_mov_b32_e32 v13, v1
	v_mov_b64_e32 v[64:65], v[14:15]
	v_mov_b64_e32 v[48:49], v[14:15]
	v_mov_b64_e32 v[32:33], v[14:15]
	v_pk_mul_f32 v[80:81], v[118:119], v[16:17] op_sel_hi:[0,1]
	v_mov_b64_e32 v[62:63], v[12:13]
	v_mov_b64_e32 v[60:61], v[10:11]
	v_mov_b64_e32 v[58:59], v[8:9]
	v_mov_b64_e32 v[56:57], v[6:7]
	v_mov_b64_e32 v[54:55], v[4:5]
	v_mov_b64_e32 v[52:53], v[2:3]
	v_mov_b64_e32 v[50:51], v[0:1]
	v_mov_b64_e32 v[46:47], v[12:13]
	v_mov_b64_e32 v[44:45], v[10:11]
	v_mov_b64_e32 v[42:43], v[8:9]
	v_mov_b64_e32 v[40:41], v[6:7]
	v_mov_b64_e32 v[38:39], v[4:5]
	v_mov_b64_e32 v[36:37], v[2:3]
	v_mov_b64_e32 v[34:35], v[0:1]
	v_mov_b64_e32 v[30:31], v[12:13]
	v_mov_b64_e32 v[28:29], v[10:11]
	v_mov_b64_e32 v[26:27], v[8:9]
	v_mov_b64_e32 v[24:25], v[6:7]
	v_mov_b64_e32 v[22:23], v[4:5]
	v_mov_b64_e32 v[20:21], v[2:3]
	v_mov_b64_e32 v[18:19], v[0:1]
	v_mov_b64_e32 v[16:17], v[14:15]
	v_mul_f32_e32 v129, 0x42000000, v118
	s_mov_b32 s28, 0
	v_lshlrev_b32_e32 v130, 8, v120
	v_lshl_add_u32 v115, v120, 2, s52
	s_add_i32 s29, 0, 0x20804
	v_mov_b64_e32 v[14:15], v[12:13]
	v_mov_b64_e32 v[12:13], v[10:11]
	v_mov_b64_e32 v[10:11], v[8:9]
	v_mov_b64_e32 v[8:9], v[6:7]
	v_mov_b64_e32 v[6:7], v[4:5]
	v_mov_b64_e32 v[4:5], v[2:3]
	v_mov_b64_e32 v[2:3], v[0:1]
	s_branch .LBB0_523

; template <int mode> __device__ __forceinline__ void attn_unit(const AttnArgs& A, const int b, const int h, const int sub, char* shm, const int wave_) {
;     ...
;     const size_t rowbase = (size_t)b * SEQ + res; const int q0 = qb * 256;
;     const bf16* Qp = A.qkv + (rowbase + (size_t)dil * ((mode == 3) ? (int)(gent & 4095u) : (q0 + wid * 32 + r32))) * QS + h * 128;
;     const bf16* Kh = A.qkv + rowbase * QS + 2048 + h * 128;
;     const bf16* Vh = A.qkv + rowbase * QS + 4096 + h * 128;
;     const size_t rstep = (size_t)dil * QS;
;     char* V_lds = shm + L_V; char* K_lds = shm + L_K;
;     float* wsf = (float*)(shm + L_WS) + wid * 64; float* li_l = wsf; float* al_l = wsf + 32;
;     int* TL = (int*)(shm + L_TL); int* FLG = (int*)(shm + L_FLG); unsigned* MSK = (unsigned*)(shm + L_MSK); float* KM = (float*)(shm + L_KM);
;     char* qf = shm + L_Q + wid * 8192 + lane * 16;
;     const int qw0 = q0 + wid * 32;
;     const int pos = qw0 + r32;
;     const int vb0 = (int)(uintptr_t)V_lds + v_rd_base(lane);
;     unsigned koffb[2], voffb[2];
; #pragma unroll
;     for (int i = 0; i < 2; ++i) { const int Lb = (2 * wid + i) * 1024 + lane * 16;
;         const int rowk = Lb >> 8, ck = ((Lb >> 4) & 15) ^ (rowk & 7);
;         koffb[i] = (unsigned)(((size_t)rowk * rstep + ck * 8) * 2);
;         const int sub_ = Lb >> 9, win_ = Lb & 511, kk = (sub_ >> 2) * 8 + (win_ >> 6), kv = (kk & ~0xC) | ((kk & 4) << 1) | ((kk & 8) >> 1), cc = (sub_ & 3) * 4 + ((win_ & 63) >> 4);
;         voffb[i] = (unsigned)(((size_t)kv * rstep + cc * 8) * 2); }
;     typedef __attribute__((address_space(3))) unsigned lds_u32;
;     lds_u32* const Kdst = (lds_u32*)(K_lds + wid * 2048); lds_u32* const Vdst = (lds_u32*)(V_lds + wid * 2048);
;     ...
;     { const int kf_ = ((mode == 3) ? gk * 256 : q0) + 192; TDMA(kf_, 0); }
;     bf16x8 qr[8];
; #pragma unroll
;     for (int d0 = 0; d0 < 8; ++d0) { qr[d0] = *reinterpret_cast<const bf16x8*>(Qp + d0 * 16 + hi * 8); *reinterpret_cast<bf16x8*>(qf + d0 * 1024) = qr[d0]; }
;     const float sl = (mode == 2) ? 0.f : __builtin_amdgcn_exp2f(-8.0f * (float)(h + 1) / 11.0f) * 1.4426950408889634f * (float)dil;
;     f32x16 binit;
; #pragma unroll
;     for (int r = 0; r < 16; ++r) binit[r] = sl * (float)((r & 3) + 8 * (r >> 2) + 4 * hi);
;     const float sl32 = 32.f * sl;
;     int NT = 0;
;     if (mode == 1) { NT = 4; if (tid < 4) TL[tid] = q0 + 192 - 64 * tid; }
.LBB0_693:
	s_and_b64 vcc, exec, s[0:1]
	s_cbranch_vccz .LBB0_436
	s_and_b32 s14, s26, 0x1c00
	s_cmpk_lg_i32 s14, 0x400
	s_cselect_b64 s[0:1], -1, 0
	s_cmpk_eq_i32 s14, 0x400
	s_cselect_b32 s22, 6, 11
	s_add_i32 s22, s22, s8
	s_cmpk_lt_u32 s26, 0x400
	s_cselect_b32 s34, s8, s22
	s_cmpk_gt_u32 s26, 0x3ff
	s_mov_b64 s[14:15], -1
	s_cbranch_scc0 .LBB0_855
	s_lshl_b32 s23, s24, 8
	v_readlane_b32 s14, v252, 37
	s_lshl_b32 s18, s25, 12
	s_add_i32 s19, s23, s14
	s_lshl_b32 s27, s22, 7
	s_mul_i32 s25, s25, 0x3000000
	s_add_u32 s14, s38, s25
	s_addc_u32 s15, s39, 0
	s_add_u32 s25, s14, 0x1000
	s_addc_u32 s30, s15, 0
	s_add_u32 s31, s14, 0x2000
	s_addc_u32 s35, s15, 0
	s_mov_b64 s[14:15], -1
	s_and_b64 vcc, exec, s[0:1]
	s_cbranch_vccz .LBB0_837
	v_mbcnt_lo_u32_b32 v0, -1, 0
	v_mbcnt_hi_u32_b32 v0, -1, v0
	v_readlane_b32 s0, v252, 28
	v_add_u32_e32 v131, s94, v0
	s_lshl_b32 s28, s27, 1
	s_waitcnt vmcnt(15)
	v_and_b32_e32 v2, 63, v131
	v_lshlrev_b32_e32 v3, 4, v2
	v_or_b32_e32 v4, s0, v3
	v_and_b32_e32 v5, 15, v131
	s_waitcnt vmcnt(14)
	v_lshrrev_b32_e32 v7, 1, v131
	v_ashrrev_i32_e32 v8, 8, v4
	v_bfe_u32 v6, v131, 2, 2
	v_and_b32_e32 v7, 8, v7
	v_readlane_b32 s0, v252, 13
	v_bitop3_b32 v9, v8, v5, 3 bitop3:0x6c
	v_mul_i32_i24_e32 v8, 0x3000, v8
	v_or3_b32 v6, v6, v7, s0
	v_and_b32_e32 v7, 3, v131
	v_lshl_or_b32 v135, v9, 4, v8
	v_lshrrev_b32_e32 v8, 3, v131
	v_mul_lo_u32 v6, v6, s70
	v_and_or_b32 v8, v8, 4, v7
	v_or_b32_e32 v4, 0x400, v4
	v_lshl_or_b32 v136, v8, 4, v6
	v_ashrrev_i32_e32 v8, 8, v4
	v_lshrrev_b32_e32 v4, 7, v4
	v_bitop3_b32 v5, v8, v5, 7 bitop3:0x6c
	v_mul_i32_i24_e32 v8, 0x3000, v8
	v_and_or_b32 v4, v4, 12, v7
	v_lshl_or_b32 v137, v5, 4, v8
	v_lshl_or_b32 v138, v4, 4, v6
	v_mov_b64_e32 v[4:5], s[38:39]
	s_add_u32 s38, s25, s28
	v_and_b32_e32 v130, 31, v131
	s_addc_u32 s39, s30, 0
	v_or_b32_e32 v134, s19, v130
	s_add_u32 s56, s31, s28
	v_add_u32_e32 v0, s18, v134
	s_addc_u32 s57, s35, 0
	s_or_b32 s14, s23, 0xc0
	v_mad_u64_u32 v[4:5], s[0:1], v0, s70, v[4:5]
	s_mul_i32 s15, s14, 0x3000
	s_add_u32 s0, s38, s15
	s_addc_u32 s1, s39, 0
	s_add_u32 s40, s56, s15
	s_addc_u32 s41, s57, 0
	v_mov_b32_e32 v0, v135
	v_mov_b32_e32 v6, v136
	s_add_i32 m0, s2, 0x8000
	s_mov_b32 s29, s90
	global_load_lds_dwordx4 v0, s[0:1]
	s_mov_b32 m0, s2
	v_mov_b32_e32 v0, v137
	global_load_lds_dwordx4 v6, s[40:41]
	v_mov_b32_e32 v6, v138
	s_add_i32 m0, s2, 0x8400
	v_bfe_u32 v132, v131, 5, 1
	global_load_lds_dwordx4 v0, s[0:1]
	v_lshl_add_u64 v[4:5], v[4:5], 0, s[28:29]
	v_lshlrev_b32_e32 v0, 4, v132
	s_add_i32 m0, s2, 0x400
	v_lshl_add_u64 v[8:9], v[4:5], 0, v[0:1]
	global_load_lds_dwordx4 v6, s[40:41]
	global_load_dwordx4 v[4:7], v[8:9], off
	global_load_dwordx4 v[12:15], v[8:9], off offset:32
	global_load_dwordx4 v[16:19], v[8:9], off offset:64
	global_load_dwordx4 v[20:23], v[8:9], off offset:96
	global_load_dwordx4 v[24:27], v[8:9], off offset:128
	global_load_dwordx4 v[28:31], v[8:9], off offset:160
	global_load_dwordx4 v[32:35], v[8:9], off offset:192
	global_load_dwordx4 v[36:39], v[8:9], off offset:224
	v_readlane_b32 s0, v252, 15
	s_nop 1
	v_add_u32_e32 v139, s0, v3
	s_add_i32 s0, s23, 0x100
	s_lshr_b32 s29, s0, 6
	v_cmp_gt_i32_e32 vcc, s29, v131
	s_waitcnt vmcnt(0)
	ds_write_b128 v139, v[4:7]
	ds_write_b128 v139, v[12:15] offset:1024
	ds_write_b128 v139, v[16:19] offset:2048
	ds_write_b128 v139, v[20:23] offset:3072
	ds_write_b128 v139, v[24:27] offset:4096
	ds_write_b128 v139, v[28:31] offset:5120
	ds_write_b128 v139, v[32:35] offset:6144
	ds_write_b128 v139, v[36:39] offset:7168
	s_and_saveexec_b64 s[0:1], vcc
	v_lshl_add_u32 v4, v131, 2, 0
	v_lshlrev_b32_e32 v5, 6, v131
	v_add_u32_e32 v4, 0x20800, v4
	v_sub_u32_e32 v5, s14, v5
	ds_write_b32 v4, v5
	s_or_b64 exec, exec, s[0:1]
	v_mov_b32_e32 v6, 0xf149f2ca
	v_mov_b32_e32 v7, v1
	v_mov_b32_e32 v119, v1
	s_waitcnt lgkmcnt(0)
	s_barrier
	s_movk_i32 s0, 0x70
	v_lshlrev_b32_e32 v6, 4, v130
	v_lshlrev_b32_e32 v5, 1, v2
	s_add_i32 s73, s19, 32
	v_and_b32_e32 v7, 0x70, v6
	v_bitop3_b32 v141, v0, v6, s0 bitop3:0x78
	s_movk_i32 s0, 0x60
	v_lshlrev_b32_e32 v4, 3, v2
	v_and_b32_e32 v5, 32, v5
	v_bitop3_b32 v144, v0, v7, s0 bitop3:0x36
	s_movk_i32 s0, 0x118
	s_cmp_lg_u32 0, -1
	v_and_b32_e32 v3, 0xc0, v3
	v_bitop3_b32 v142, v0, v7, 32 bitop3:0x36
	v_bitop3_b32 v143, v0, v7, 64 bitop3:0x36
	v_and_or_b32 v0, v4, s0, v5
	s_cselect_b32 s0, 0, 0
	v_mov_b32_e32 v14, v1
	v_mov_b32_e32 v15, v1
	v_cmp_gt_u32_e64 s[40:41], 32, v2
	v_cmp_eq_u32_e64 s[42:43], 0, v2
	v_add3_u32 v146, v3, s0, v0
	v_mov_b32_e32 v0, v1
	v_mov_b32_e32 v2, v1
	v_mov_b32_e32 v3, v1
	v_mov_b32_e32 v4, v1
	v_mov_b32_e32 v5, v1
	v_mov_b32_e32 v6, v1
	v_mov_b32_e32 v7, v1
	v_mov_b32_e32 v8, v1
	v_mov_b32_e32 v9, v1
	v_mov_b32_e32 v10, v1
	v_mov_b32_e32 v11, v1
	v_mov_b32_e32 v12, v1
	v_mov_b32_e32 v13, v1
	v_mov_b64_e32 v[64:65], v[14:15]
	v_mov_b64_e32 v[48:49], v[14:15]
	v_mov_b64_e32 v[32:33], v[14:15]
	v_mov_b64_e32 v[62:63], v[12:13]
	v_mov_b64_e32 v[60:61], v[10:11]
	v_mov_b64_e32 v[58:59], v[8:9]
	v_mov_b64_e32 v[56:57], v[6:7]
	v_mov_b64_e32 v[54:55], v[4:5]
	v_mov_b64_e32 v[52:53], v[2:3]
	v_mov_b64_e32 v[50:51], v[0:1]
	v_mov_b64_e32 v[46:47], v[12:13]
	v_mov_b64_e32 v[44:45], v[10:11]
	v_mov_b64_e32 v[42:43], v[8:9]
	v_mov_b64_e32 v[40:41], v[6:7]
	v_mov_b64_e32 v[38:39], v[4:5]
	v_mov_b64_e32 v[36:37], v[2:3]
	v_mov_b64_e32 v[34:35], v[0:1]
	v_mov_b64_e32 v[30:31], v[12:13]
	v_mov_b64_e32 v[28:29], v[10:11]
	v_mov_b64_e32 v[26:27], v[8:9]
	v_mov_b64_e32 v[24:25], v[6:7]
	v_mov_b64_e32 v[22:23], v[4:5]
	v_mov_b64_e32 v[20:21], v[2:3]
	v_mov_b64_e32 v[18:19], v[0:1]
	v_mov_b64_e32 v[16:17], v[14:15]
	s_mov_b32 s72, 0
	v_lshlrev_b32_e32 v140, 8, v130
	v_lshlrev_b32_e32 v145, 2, v132
	s_add_i32 s74, 0, 0x20804
	s_mov_b64 s[44:45], 0
	v_mov_b64_e32 v[14:15], v[12:13]
	v_mov_b64_e32 v[12:13], v[10:11]
	v_mov_b64_e32 v[10:11], v[8:9]
	v_mov_b64_e32 v[8:9], v[6:7]
	v_mov_b64_e32 v[6:7], v[4:5]
	v_mov_b64_e32 v[4:5], v[2:3]
	v_mov_b64_e32 v[2:3], v[0:1]
	s_branch .LBB0_700

; template <int mode> __device__ __forceinline__ void attn_unit(const AttnArgs& A, const int b, const int h, const int sub, char* shm, const int wave_) {
;     ...
;     const size_t rowbase = (size_t)b * SEQ + res; const int q0 = qb * 256;
;     const bf16* Qp = A.qkv + (rowbase + (size_t)dil * ((mode == 3) ? (int)(gent & 4095u) : (q0 + wid * 32 + r32))) * QS + h * 128;
;     const bf16* Kh = A.qkv + rowbase * QS + 2048 + h * 128;
;     const bf16* Vh = A.qkv + rowbase * QS + 4096 + h * 128;
;     const size_t rstep = (size_t)dil * QS;
;     char* V_lds = shm + L_V; char* K_lds = shm + L_K;
;     float* wsf = (float*)(shm + L_WS) + wid * 64; float* li_l = wsf; float* al_l = wsf + 32;
;     int* TL = (int*)(shm + L_TL); int* FLG = (int*)(shm + L_FLG); unsigned* MSK = (unsigned*)(shm + L_MSK); float* KM = (float*)(shm + L_KM);
;     char* qf = shm + L_Q + wid * 8192 + lane * 16;
;     const int qw0 = q0 + wid * 32;
;     const int pos = qw0 + r32;
;     const int vb0 = (int)(uintptr_t)V_lds + v_rd_base(lane);
;     unsigned koffb[2], voffb[2];
; #pragma unroll
;     for (int i = 0; i < 2; ++i) { const int Lb = (2 * wid + i) * 1024 + lane * 16;
;         const int rowk = Lb >> 8, ck = ((Lb >> 4) & 15) ^ (rowk & 7);
;         koffb[i] = (unsigned)(((size_t)rowk * rstep + ck * 8) * 2);
;         const int sub_ = Lb >> 9, win_ = Lb & 511, kk = (sub_ >> 2) * 8 + (win_ >> 6), kv = (kk & ~0xC) | ((kk & 4) << 1) | ((kk & 8) >> 1), cc = (sub_ & 3) * 4 + ((win_ & 63) >> 4);
;         voffb[i] = (unsigned)(((size_t)kv * rstep + cc * 8) * 2); }
;     typedef __attribute__((address_space(3))) unsigned lds_u32;
;     lds_u32* const Kdst = (lds_u32*)(K_lds + wid * 2048); lds_u32* const Vdst = (lds_u32*)(V_lds + wid * 2048);
;     ...
;     { const int kf_ = ((mode == 3) ? gk * 256 : q0) + 192; TDMA(kf_, 0); }
;     bf16x8 qr[8];
; #pragma unroll
;     for (int d0 = 0; d0 < 8; ++d0) { qr[d0] = *reinterpret_cast<const bf16x8*>(Qp + d0 * 16 + hi * 8); *reinterpret_cast<bf16x8*>(qf + d0 * 1024) = qr[d0]; }
;     const float sl = (mode == 2) ? 0.f : __builtin_amdgcn_exp2f(-8.0f * (float)(h + 1) / 11.0f) * 1.4426950408889634f * (float)dil;
;     f32x16 binit;
; #pragma unroll
;     for (int r = 0; r < 16; ++r) binit[r] = sl * (float)((r & 3) + 8 * (r >> 2) + 4 * hi);
;     const float sl32 = 32.f * sl;
;     int NT = 0;
;     if (mode == 1) { NT = 4; if (tid < 4) TL[tid] = q0 + 192 - 64 * tid; }
.LBB0_837:
	s_and_b64 vcc, exec, s[14:15]
	s_cbranch_vccz .LBB0_854
	v_mbcnt_lo_u32_b32 v0, -1, 0
	v_mbcnt_hi_u32_b32 v0, -1, v0
	v_readlane_b32 s0, v252, 28
	v_add_u32_e32 v134, s94, v0
	s_lshl_b32 s28, s27, 1
	s_waitcnt vmcnt(15)
	v_and_b32_e32 v2, 63, v134
	v_lshlrev_b32_e32 v3, 4, v2
	v_or_b32_e32 v4, s0, v3
	v_and_b32_e32 v5, 15, v134
	s_waitcnt vmcnt(14)
	v_lshrrev_b32_e32 v7, 1, v134
	v_ashrrev_i32_e32 v8, 8, v4
	v_bfe_u32 v6, v134, 2, 2
	v_and_b32_e32 v7, 8, v7
	v_readlane_b32 s0, v252, 13
	v_bitop3_b32 v9, v8, v5, 3 bitop3:0x6c
	v_mul_i32_i24_e32 v8, 0x3000, v8
	v_or3_b32 v6, v6, v7, s0
	v_and_b32_e32 v7, 3, v134
	v_lshl_or_b32 v150, v9, 4, v8
	v_lshrrev_b32_e32 v8, 3, v134
	v_mul_lo_u32 v6, v6, s70
	v_and_or_b32 v8, v8, 4, v7
	v_or_b32_e32 v4, 0x400, v4
	s_add_u32 s14, s25, s28
	v_and_b32_e32 v126, 31, v134
	v_lshl_or_b32 v152, v8, 4, v6
	v_ashrrev_i32_e32 v8, 8, v4
	v_lshrrev_b32_e32 v4, 7, v4
	s_addc_u32 s15, s30, 0
	v_or_b32_e32 v139, s19, v126
	v_bitop3_b32 v5, v8, v5, 7 bitop3:0x6c
	v_mul_i32_i24_e32 v8, 0x3000, v8
	v_and_or_b32 v4, v4, 12, v7
	s_add_u32 s25, s31, s28
	v_add_u32_e32 v0, s18, v139
	v_lshl_or_b32 v154, v5, 4, v8
	v_lshl_or_b32 v156, v4, 4, v6
	v_mov_b64_e32 v[4:5], s[38:39]
	s_addc_u32 s27, s35, 0
	s_or_b32 s23, s23, 0xc0
	v_mad_u64_u32 v[4:5], s[0:1], v0, s70, v[4:5]
	s_mul_i32 s30, s23, 0x3000
	s_add_u32 s0, s14, s30
	s_addc_u32 s1, s15, 0
	s_add_u32 s30, s25, s30
	s_addc_u32 s31, s27, 0
	v_mov_b32_e32 v0, v152
	v_mov_b32_e32 v6, v150
	s_add_i32 m0, s2, 0x8000
	s_mov_b32 s29, s90
	global_load_lds_dwordx4 v6, s[0:1]
	s_mov_b32 m0, s2
	v_mov_b32_e32 v6, v154
	global_load_lds_dwordx4 v0, s[30:31]
	v_mov_b32_e32 v0, v156
	s_add_i32 m0, s2, 0x8400
	v_bfe_u32 v135, v134, 5, 1
	global_load_lds_dwordx4 v6, s[0:1]
	s_add_i32 m0, s2, 0x400
	v_lshl_add_u64 v[4:5], v[4:5], 0, s[28:29]
	global_load_lds_dwordx4 v0, s[30:31]
	v_lshlrev_b32_e32 v0, 4, v135
	v_lshl_add_u64 v[8:9], v[4:5], 0, v[0:1]
	global_load_dwordx4 v[4:7], v[8:9], off
	global_load_dwordx4 v[12:15], v[8:9], off offset:32
	global_load_dwordx4 v[16:19], v[8:9], off offset:64
	global_load_dwordx4 v[20:23], v[8:9], off offset:96
	global_load_dwordx4 v[24:27], v[8:9], off offset:128
	global_load_dwordx4 v[28:31], v[8:9], off offset:160
	global_load_dwordx4 v[32:35], v[8:9], off offset:192
	global_load_dwordx4 v[36:39], v[8:9], off offset:224
	v_readlane_b32 s0, v252, 15
	v_cmp_gt_i32_e32 vcc, 4, v134
	s_nop 0
	v_add_u32_e32 v140, s0, v3
	s_waitcnt vmcnt(0)
	ds_write_b128 v140, v[4:7]
	ds_write_b128 v140, v[12:15] offset:1024
	ds_write_b128 v140, v[16:19] offset:2048
	ds_write_b128 v140, v[20:23] offset:3072
	ds_write_b128 v140, v[24:27] offset:4096
	ds_write_b128 v140, v[28:31] offset:5120
	ds_write_b128 v140, v[32:35] offset:6144
	ds_write_b128 v140, v[36:39] offset:7168
	s_and_saveexec_b64 s[0:1], vcc
	v_lshl_add_u32 v4, v134, 2, 0
	v_lshlrev_b32_e32 v5, 6, v134
	v_add_u32_e32 v4, 0x20800, v4
	v_sub_u32_e32 v5, s23, v5
	ds_write_b32 v4, v5
	s_or_b64 exec, exec, s[0:1]
	s_not_b32 s0, s22
	s_lshl_b32 s0, s0, 3
	v_cvt_f32_i32_e32 v4, s0
	s_mov_b32 s22, 0x41300000
	v_lshlrev_b32_e32 v142, 2, v135
	v_or_b32_e32 v129, 3, v142
	v_div_scale_f32 v5, s[0:1], s22, s22, v4
	v_rcp_f32_e32 v6, v5
	v_div_scale_f32 v7, vcc, v4, s22, v4
	v_or_b32_e32 v128, 2, v142
	v_fma_f32 v8, -v5, v6, 1.0
	v_fmac_f32_e32 v6, v8, v6
	v_mul_f32_e32 v8, v7, v6
	v_fma_f32 v9, -v5, v8, v7
	v_fmac_f32_e32 v8, v9, v6
	v_fma_f32 v5, -v5, v8, v7
	v_div_fmas_f32 v5, v5, v6, v8
	v_div_fixup_f32 v4, v5, s22, v4
	v_exp_f32_e32 v4, v4
	v_cvt_f32_ubyte0_e32 v5, v129
	v_lshlrev_b32_e32 v21, 1, v2
	v_mov_b32_e32 v130, 0xf149f2ca
	v_mul_f32_e32 v132, 0x3fb8aa3b, v4
	v_cvt_f32_ubyte0_e32 v4, v128
	v_pk_mul_f32 v[68:69], v[132:133], v[4:5] op_sel_hi:[0,1]
	v_mov_b32_e32 v131, v1
	v_mov_b32_e32 v5, v1
	v_lshlrev_b32_e32 v20, 3, v2
	v_or_b32_e32 v125, 9, v142
	v_or_b32_e32 v124, 8, v142
	v_and_b32_e32 v4, 32, v21
	s_waitcnt lgkmcnt(0)
	s_barrier
; #define tid (tid_of(wave))
; template <int mode> __device__ __forceinline__ void attn_unit(const AttnArgs& A, const int b, const int h, const int sub, char* shm, const int wave_) {
;     ...
;     const float sl = (mode == 2) ? 0.f : __builtin_amdgcn_exp2f(-8.0f * (float)(h + 1) / 11.0f) * 1.4426950408889634f * (float)dil;
;     f32x16 binit;
; #pragma unroll
;     for (int r = 0; r < 16; ++r) binit[r] = sl * (float)((r & 3) + 8 * (r >> 2) + 4 * hi);
;     const float sl32 = 32.f * sl;
;     int NT = 0;
;     if (mode == 1) { NT = 4; if (tid < 4) TL[tid] = q0 + 192 - 64 * tid; }
;     else if (mode == 3) { NT = 4; if (tid < 4) TL[tid] = gk * 256 + 192 - 64 * tid; }
;     else if (mode == 0) {
;         const int lo = q0 >= 128 ? q0 - 128 : 0; NT = (q0 + 256 - lo) / 64;
;         if (tid < NT) TL[NT - 1 - tid] = lo + 64 * tid;
;     } else {
;         NT = (q0 + 256) / 64;
;         if (tid < NT) TL[tid] = q0 + 192 - 64 * tid;
;     }
;     __syncthreads();
;     float m_reg = -1e30f, l_reg = 0.f, carry = 0.f; asm volatile("" : "+v"(m_reg), "+v"(l_reg), "+v"(carry));
;     f32x16 o[4];
; #pragma unroll
;     for (int d0 = 0; d0 < 4; ++d0) o[d0] = f32x16{};
;     bool wdone = false;
	s_movk_i32 s0, 0x118
	v_or_b32_e32 v117, 25, v142
	v_or_b32_e32 v116, 24, v142
	v_cvt_f32_ubyte0_e32 v7, v125
	v_cvt_f32_ubyte0_e32 v6, v124
	v_and_or_b32 v4, v20, s0, v4
	s_or_b32 s23, s19, 31
	v_lshlrev_b32_e32 v5, 4, v126
	s_movk_i32 s0, 0x70
	v_or_b32_e32 v136, 1, v142
	v_or_b32_e32 v123, 11, v142
	v_or_b32_e32 v122, 10, v142
	v_or_b32_e32 v121, 17, v142
	v_or_b32_e32 v120, 16, v142
	v_or_b32_e32 v119, 19, v142
	v_or_b32_e32 v118, 18, v142
	v_cvt_f32_ubyte0_e32 v15, v117
	v_cvt_f32_ubyte0_e32 v14, v116
	v_pk_mul_f32 v[70:71], v[132:133], v[6:7] op_sel_hi:[0,1]
	v_and_b32_e32 v6, 0x70, v5
	v_bitop3_b32 v173, v0, v5, s0 bitop3:0x78
	s_movk_i32 s0, 0x60
	s_cmp_lg_u32 0, -1
	v_and_b32_e32 v3, 0xc0, v3
	v_or_b32_e32 v115, 27, v142
	v_or_b32_e32 v114, 26, v142
	v_cvt_f32_ubyte0_e32 v9, v123
	v_cvt_f32_ubyte0_e32 v8, v122
	v_cvt_f32_ubyte0_e32 v11, v121
	v_cvt_f32_ubyte0_e32 v10, v120
	v_cvt_f32_ubyte0_e32 v13, v119
	v_cvt_f32_ubyte0_e32 v12, v118
	v_cvt_f32_ubyte0_e32 v18, v142
	v_cvt_f32_ubyte0_e32 v19, v136
	v_pk_mul_f32 v[78:79], v[132:133], v[14:15] op_sel_hi:[0,1]
	v_bitop3_b32 v170, v0, v6, s0 bitop3:0x36
	s_cselect_b32 s0, 0, 0
	v_mov_b32_e32 v14, v1
	v_mov_b32_e32 v15, v1
	v_cvt_f32_ubyte0_e32 v17, v115
	v_cvt_f32_ubyte0_e32 v16, v114
	v_pk_mul_f32 v[76:77], v[132:133], v[12:13] op_sel_hi:[0,1]
	v_pk_mul_f32 v[74:75], v[132:133], v[10:11] op_sel_hi:[0,1]
	v_pk_mul_f32 v[72:73], v[132:133], v[8:9] op_sel_hi:[0,1]
	v_pk_mul_f32 v[66:67], v[132:133], v[18:19] op_sel_hi:[0,1]
	v_bitop3_b32 v172, v0, v6, 32 bitop3:0x36
	v_bitop3_b32 v171, v0, v6, 64 bitop3:0x36
	v_cmp_gt_u32_e64 s[42:43], 32, v2
	v_cmp_lt_u32_e64 s[40:41], 31, v2
	v_add3_u32 v127, v3, s0, v4
	v_add_u32_e32 v137, s52, v0
	v_mov_b32_e32 v0, v1
	v_mov_b32_e32 v2, v1
	v_mov_b32_e32 v3, v1
	v_mov_b32_e32 v4, v1
	v_mov_b32_e32 v5, v1
	v_mov_b32_e32 v6, v1
	v_mov_b32_e32 v7, v1
	v_mov_b32_e32 v8, v1
	v_mov_b32_e32 v9, v1
	v_mov_b32_e32 v10, v1
	v_mov_b32_e32 v11, v1
	v_mov_b32_e32 v12, v1
	v_mov_b32_e32 v13, v1
	v_mov_b64_e32 v[64:65], v[14:15]
	v_mov_b64_e32 v[48:49], v[14:15]
	v_mov_b64_e32 v[32:33], v[14:15]
	v_pk_mul_f32 v[80:81], v[132:133], v[16:17] op_sel_hi:[0,1]
	v_mov_b64_e32 v[62:63], v[12:13]
	v_mov_b64_e32 v[60:61], v[10:11]
	v_mov_b64_e32 v[58:59], v[8:9]
	v_mov_b64_e32 v[56:57], v[6:7]
	v_mov_b64_e32 v[54:55], v[4:5]
	v_mov_b64_e32 v[52:53], v[2:3]
	v_mov_b64_e32 v[50:51], v[0:1]
	v_mov_b64_e32 v[46:47], v[12:13]
	v_mov_b64_e32 v[44:45], v[10:11]
	v_mov_b64_e32 v[42:43], v[8:9]
	v_mov_b64_e32 v[40:41], v[6:7]
	v_mov_b64_e32 v[38:39], v[4:5]
	v_mov_b64_e32 v[36:37], v[2:3]
	v_mov_b64_e32 v[34:35], v[0:1]
	v_mov_b64_e32 v[30:31], v[12:13]
	v_mov_b64_e32 v[28:29], v[10:11]
	v_mov_b64_e32 v[26:27], v[8:9]
	v_mov_b64_e32 v[24:25], v[6:7]
	v_mov_b64_e32 v[22:23], v[4:5]
	v_mov_b64_e32 v[20:21], v[2:3]
	v_mov_b64_e32 v[18:19], v[0:1]
	v_mov_b64_e32 v[16:17], v[14:15]
	v_mul_f32_e32 v141, 0x42000000, v132
	s_mov_b32 s22, 0
	v_lshlrev_b32_e32 v161, 8, v126
	v_lshl_add_u32 v138, v126, 2, s52
	v_add_u32_e32 v160, -2, v139
	v_add_u32_e32 v159, -3, v139
	v_add_u32_e32 v158, -8, v139
	v_add_u32_e32 v157, -9, v139
	v_add_u32_e32 v155, -10, v139
	v_add_u32_e32 v153, -11, v139
	v_add_u32_e32 v151, -16, v139
	v_subrev_u32_e32 v149, 17, v139
	v_subrev_u32_e32 v148, 18, v139
	v_subrev_u32_e32 v147, 19, v139
	v_subrev_u32_e32 v146, 24, v139
	v_subrev_u32_e32 v145, 25, v139
	v_subrev_u32_e32 v144, 26, v139
	v_subrev_u32_e32 v143, 27, v139
	s_sub_i32 s29, s19, 63
	s_add_i32 s30, 0, 0x20804
	v_mov_b64_e32 v[14:15], v[12:13]
	v_mov_b64_e32 v[12:13], v[10:11]
	v_mov_b64_e32 v[10:11], v[8:9]
	v_mov_b64_e32 v[8:9], v[6:7]
	v_mov_b64_e32 v[6:7], v[4:5]
	v_mov_b64_e32 v[4:5], v[2:3]
	v_mov_b64_e32 v[2:3], v[0:1]
	s_branch .LBB0_844

; #define lane (lane_id())
; template <int mode> __device__ __forceinline__ void attn_unit(const AttnArgs& A, const int b, const int h, const int sub, char* shm, const int wave_) {
;     ...
;     if (mode == 0) { br = sub >> 4; const int x = sub & 15; if (br == 0) { qb = x; } else if (br == 1) { dil = 4; res = x >> 2; qb = x & 3; } else { dil = 16; res = x; qb = 0; } }
;     if (mode == 3) { gk = sub >> 4; const int c = sub & 15; const int li = (b * 5 + (h - 6)) * 15 + gk;
;         gcnt = __builtin_amdgcn_readfirstlane((int)ld_sc1(A.mcnt + li));
;         if (c * 256 >= gcnt) return;
;         const int gi = c * 256 + wid * 32 + r32; gvalid = gi < gcnt; wvalid = (c * 256 + wid * 32) < gcnt;
;         gent = ld_sc1(A.mlist + (size_t)li * MLCAP + (gvalid ? gi : 0)); qb = 0; }
;     const size_t rowbase = (size_t)b * SEQ + res; const int q0 = qb * 256;
;     const bf16* Qp = A.qkv + (rowbase + (size_t)dil * ((mode == 3) ? (int)(gent & 4095u) : (q0 + wid * 32 + r32))) * QS + h * 128;
;     const bf16* Kh = A.qkv + rowbase * QS + 2048 + h * 128;
;     const bf16* Vh = A.qkv + rowbase * QS + 4096 + h * 128;
;     const size_t rstep = (size_t)dil * QS;
;     char* V_lds = shm + L_V; char* K_lds = shm + L_K;
;     float* wsf = (float*)(shm + L_WS) + wid * 64; float* li_l = wsf; float* al_l = wsf + 32;
;     int* TL = (int*)(shm + L_TL); int* FLG = (int*)(shm + L_FLG); unsigned* MSK = (unsigned*)(shm + L_MSK); float* KM = (float*)(shm + L_KM);
;     char* qf = shm + L_Q + wid * 8192 + lane * 16;
;     const int qw0 = q0 + wid * 32;
;     const int pos = qw0 + r32;
;     const int vb0 = (int)(uintptr_t)V_lds + v_rd_base(lane);
;     unsigned koffb[2], voffb[2];
; #pragma unroll
;     for (int i = 0; i < 2; ++i) { const int Lb = (2 * wid + i) * 1024 + lane * 16;
;         const int rowk = Lb >> 8, ck = ((Lb >> 4) & 15) ^ (rowk & 7);
;         koffb[i] = (unsigned)(((size_t)rowk * rstep + ck * 8) * 2);
;         const int sub_ = Lb >> 9, win_ = Lb & 511, kk = (sub_ >> 2) * 8 + (win_ >> 6), kv = (kk & ~0xC) | ((kk & 4) << 1) | ((kk & 8) >> 1), cc = (sub_ & 3) * 4 + ((win_ & 63) >> 4);
;         voffb[i] = (unsigned)(((size_t)kv * rstep + cc * 8) * 2); }
;     typedef __attribute__((address_space(3))) unsigned lds_u32;
;     lds_u32* const Kdst = (lds_u32*)(K_lds + wid * 2048); lds_u32* const Vdst = (lds_u32*)(V_lds + wid * 2048);
.LBB0_870:
	s_lshl_b32 s1, s1, 12
	s_or_b32 s24, s14, s1
	s_lshl_b32 s1, s0, 8
	v_readlane_b32 s14, v252, 37
	v_and_b32_e32 v144, 31, v142
	s_mov_b32 s25, s90
	s_add_i32 s22, s1, s14
	v_or_b32_e32 v147, s22, v144
	s_waitcnt vmcnt(15)
	v_mov_b64_e32 v[2:3], s[24:25]
	v_mad_u64_u32 v[4:5], s[14:15], v147, s18, v[2:3]
	s_mul_i32 s15, s24, 0x3000
	v_and_b32_e32 v149, 63, v142
	s_mul_hi_u32 s14, s24, 0x3000
	s_add_u32 s25, s38, s15
	s_addc_u32 s26, s39, s14
	v_lshlrev_b32_e32 v2, 4, v149
	v_readlane_b32 s14, v252, 28
	s_mul_i32 s23, s18, 0x1800
	s_waitcnt vmcnt(14)
	v_lshrrev_b32_e32 v7, 1, v142
	v_or_b32_e32 v0, s14, v2
	v_and_b32_e32 v3, 15, v142
	s_lshl_b32 s14, s23, 1
	v_bfe_u32 v6, v142, 2, 2
	v_and_b32_e32 v7, 8, v7
	v_readlane_b32 s15, v252, 13
	v_ashrrev_i32_e32 v8, 8, v0
	v_bitop3_b32 v9, v8, v3, 3 bitop3:0x6c
	v_or3_b32 v6, v6, v7, s15
	v_mul_i32_i24_e32 v8, s14, v8
	v_and_b32_e32 v7, 3, v142
	v_mul_lo_u32 v6, v6, s23
	v_lshl_or_b32 v151, v9, 4, v8
	v_lshrrev_b32_e32 v8, 3, v142
	v_lshlrev_b32_e32 v6, 1, v6
	v_and_or_b32 v8, v8, 4, v7
	v_or_b32_e32 v0, 0x400, v0
	v_lshl_or_b32 v152, v8, 4, v6
	v_ashrrev_i32_e32 v8, 8, v0
	v_lshrrev_b32_e32 v0, 7, v0
	v_and_or_b32 v0, v0, 12, v7
	v_lshl_or_b32 v154, v0, 4, v6
	v_mov_b64_e32 v[6:7], s[38:39]
	v_bitop3_b32 v3, v8, v3, 7 bitop3:0x6c
	v_mul_i32_i24_e32 v8, s14, v8
	v_mad_u64_u32 v[6:7], s[14:15], v4, s70, v[6:7]
	s_lshl_b32 s14, s8, 8
	s_add_u32 s27, s25, s14
	s_addc_u32 s28, s26, 0
	s_add_u32 s25, s27, 0x1000
	s_addc_u32 s26, s28, 0
	s_add_u32 s27, s27, 0x2000
	s_addc_u32 s28, s28, 0
	s_or_b32 s29, s1, 0xc0
	s_mul_i32 s29, s23, s29
	s_lshl_b32 s29, s29, 1
	s_add_u32 s30, s25, s29
	s_addc_u32 s31, s26, 0
	s_add_u32 s38, s27, s29
	v_lshl_or_b32 v153, v3, 4, v8
	s_addc_u32 s39, s28, 0
	v_mov_b32_e32 v0, v151
	v_mov_b32_e32 v3, v152
	s_add_i32 m0, s2, 0x8000
	v_bfe_u32 v145, v142, 5, 1
	global_load_lds_dwordx4 v0, s[30:31]
	s_mov_b32 m0, s2
	v_mov_b32_e32 v0, v153
	global_load_lds_dwordx4 v3, s[38:39]
	v_mov_b32_e32 v3, v154
	v_mad_u32_u24 v7, v5, s70, v7
	s_mov_b32 s15, s90
	s_add_i32 m0, s2, 0x8400
	v_lshl_add_u64 v[4:5], v[6:7], 0, s[14:15]
	global_load_lds_dwordx4 v0, s[30:31]
	v_lshlrev_b32_e32 v0, 4, v145
	v_lshl_add_u64 v[8:9], v[4:5], 0, v[0:1]
	global_load_dwordx4 v[4:7], v[8:9], off
	global_load_dwordx4 v[12:15], v[8:9], off offset:32
	global_load_dwordx4 v[16:19], v[8:9], off offset:64
	global_load_dwordx4 v[20:23], v[8:9], off offset:96
	global_load_dwordx4 v[24:27], v[8:9], off offset:128
	global_load_dwordx4 v[28:31], v[8:9], off offset:160
	global_load_dwordx4 v[32:35], v[8:9], off offset:192
	global_load_dwordx4 v[36:39], v[8:9], off offset:224
	v_readlane_b32 s14, v252, 15
	s_add_i32 m0, s2, 0x400
	s_nop 0
	v_add_u32_e32 v156, s14, v2
	global_load_lds_dwordx4 v3, s[38:39]
	s_add_i32 s14, s1, 0xffffff80
	s_cmp_lg_u32 s0, 0
	s_cselect_b32 s14, s14, 0
	s_sub_i32 s0, s1, s14
	s_addk_i32 s0, 0x100
	s_ashr_i32 s29, s0, 6
	v_cmp_gt_i32_e32 vcc, s29, v142
	s_waitcnt vmcnt(0)
	ds_write_b128 v156, v[4:7]
	ds_write_b128 v156, v[12:15] offset:1024
	ds_write_b128 v156, v[16:19] offset:2048
	ds_write_b128 v156, v[20:23] offset:3072
	ds_write_b128 v156, v[24:27] offset:4096
	ds_write_b128 v156, v[28:31] offset:5120
	ds_write_b128 v156, v[32:35] offset:6144
	ds_write_b128 v156, v[36:39] offset:7168
	s_and_saveexec_b64 s[0:1], vcc
	s_cbranch_execz .LBB0_872
	s_lshl_b32 s15, s29, 2
	s_add_i32 s15, s15, 0
	v_not_b32_e32 v3, v142
	v_lshl_add_u32 v3, v3, 2, s15
	v_add_u32_e32 v3, 0x20800, v3
	v_lshl_add_u32 v4, v142, 6, s14
	ds_write_b32 v3, v4

; __device__ __forceinline__ unsigned cvt_pk_bf16(float lo, float hi) { unsigned r; asm volatile("v_cvt_pk_bf16_f32 %0, %1, %2" : "=v"(r) : "v"(lo), "v"(hi)); return r; }
;     __device__ __forceinline__ void operator()(const f32x4 (&acc)[2][2][4][2], const Unit& u, int wr, int wc, int fr, int fq) const {
;         const int row0 = u.pm * BM + wr * 64 + fr, col0 = u.pn * BM + wc * 32 + 8 * fq;
; #pragma unroll
;         for (int ai = 0; ai < 2; ++ai)
; #pragma unroll
;             for (int m = 0; m < 4; ++m) { const size_t off = (size_t)(row0 + ai * HALF + m * 16) * ldc + col0; float sq_ = 0.f;
; #pragma unroll
;                 for (int bj = 0; bj < 2; ++bj) { f32x4 v0 = acc[ai][bj][m][0], v1 = acc[ai][bj][m][1];
;                     if (base32) { v0 += *(const f32x4*)(base32 + off + bj * HALF); v1 += *(const f32x4*)(base32 + off + bj * HALF + 4); }
;                     else if (base16) { const u32x4 b = *(const u32x4*)(base16 + off + bj * HALF);
;                         v0 += (f32x4){__uint_as_float(b.x << 16), __uint_as_float(b.x & 0xffff0000u), __uint_as_float(b.y << 16), __uint_as_float(b.y & 0xffff0000u)};
;                         v1 += (f32x4){__uint_as_float(b.z << 16), __uint_as_float(b.z & 0xffff0000u), __uint_as_float(b.w << 16), __uint_as_float(b.w & 0xffff0000u)}; }
;                     if (ssq) { float s_ = sq_; s_ = fmaf(v0[0], v0[0], s_); s_ = fmaf(v0[1], v0[1], s_); s_ = fmaf(v0[2], v0[2], s_); s_ = fmaf(v0[3], v0[3], s_);
;                       s_ = fmaf(v1[0], v1[0], s_); s_ = fmaf(v1[1], v1[1], s_); s_ = fmaf(v1[2], v1[2], s_); s_ = fmaf(v1[3], v1[3], s_); sq_ = s_; }
;                     u32x4 w; w.x = cvt_pk_bf16(v0[0], v0[1]); w.y = cvt_pk_bf16(v0[2], v0[3]); w.z = cvt_pk_bf16(v1[0], v1[1]); w.w = cvt_pk_bf16(v1[2], v1[3]);
;                     *(u32x4*)((u.kh ? out16b : out16) + off + bj * HALF) = w;
.LBB0_1309:
	s_lshl_b32 s18, s54, 8
	v_readlane_b32 s19, v252, 1
	v_mbcnt_lo_u32_b32 v0, -1, 0
	v_mbcnt_hi_u32_b32 v0, -1, v0
	s_add_i32 s18, s18, s19
	v_and_or_b32 v138, v0, 15, s18
	s_lshl_b32 s18, s53, 8
	v_ashrrev_i32_e32 v0, 1, v0
	v_readlane_b32 s19, v252, 3
	v_and_b32_e32 v0, -8, v0
	s_or_b32 s18, s18, s19
	v_add_u32_e32 v140, s18, v0
	v_ashrrev_i32_e32 v139, 31, v138
	v_ashrrev_i32_e32 v141, 31, v140
	v_lshlrev_b64 v[130:131], 11, v[138:139]
	v_lshl_add_u64 v[144:145], v[130:131], 0, v[140:141]
	v_cndmask_b32_e64 v0, 0, 1, s[16:17]
	v_cmp_ne_u32_e64 s[42:43], 1, v0
	v_lshl_add_u64 v[142:143], v[144:145], 2, s[14:15]
	s_and_b64 vcc, exec, s[16:17]
	s_cbranch_vccz .Lwo_pf_b16
	s_mov_b64 s[18:19], 0x0
	v_lshl_add_u64 v[152:153], v[142:143], 0, s[18:19]
	global_load_dwordx4 v[156:159], v[152:153], off offset:16
	global_load_dwordx4 v[152:155], v[152:153], off
	s_mov_b64 s[18:19], 0x0
	v_lshl_add_u64 v[160:161], v[142:143], 0, s[18:19]
	global_load_dwordx4 v[164:167], v[160:161], off offset:528
	global_load_dwordx4 v[160:163], v[160:161], off offset:512
	s_mov_b64 s[18:19], 0x20000
	v_lshl_add_u64 v[168:169], v[142:143], 0, s[18:19]
	global_load_dwordx4 v[172:175], v[168:169], off offset:16
	global_load_dwordx4 v[168:171], v[168:169], off
	s_mov_b64 s[18:19], 0x20000
	v_lshl_add_u64 v[176:177], v[142:143], 0, s[18:19]
	global_load_dwordx4 v[180:183], v[176:177], off offset:528
	global_load_dwordx4 v[176:179], v[176:177], off offset:512
	s_mov_b64 s[18:19], 0x40000
	v_lshl_add_u64 v[184:185], v[142:143], 0, s[18:19]
	global_load_dwordx4 v[188:191], v[184:185], off offset:16
	global_load_dwordx4 v[184:187], v[184:185], off
	s_mov_b64 s[18:19], 0x40000
	v_lshl_add_u64 v[192:193], v[142:143], 0, s[18:19]
	global_load_dwordx4 v[196:199], v[192:193], off offset:528
	global_load_dwordx4 v[192:195], v[192:193], off offset:512
	s_mov_b64 s[18:19], 0x60000
	v_lshl_add_u64 v[208:209], v[142:143], 0, s[18:19]
	global_load_dwordx4 v[212:215], v[208:209], off offset:16
	global_load_dwordx4 v[208:211], v[208:209], off
	s_mov_b64 s[18:19], 0x60000
	v_lshl_add_u64 v[216:217], v[142:143], 0, s[18:19]
	global_load_dwordx4 v[220:223], v[216:217], off offset:528
	global_load_dwordx4 v[216:219], v[216:217], off offset:512
	s_branch .Lwo_pf_done
.Lwo_pf_b16:
	s_and_b64 vcc, exec, s[12:13]
	s_cbranch_vccz .Lwo_pf_done
	v_lshl_add_u64 v[130:131], v[144:145], 1, s[0:1]
	s_mov_b64 s[18:19], 0x0
	v_lshl_add_u64 v[152:153], v[130:131], 0, s[18:19]
	global_load_dwordx4 v[152:155], v[152:153], off
	s_mov_b64 s[18:19], 0x0
	v_lshl_add_u64 v[156:157], v[130:131], 0, s[18:19]
	global_load_dwordx4 v[156:159], v[156:157], off offset:256
	s_mov_b64 s[18:19], 0x10000
	v_lshl_add_u64 v[160:161], v[130:131], 0, s[18:19]
	global_load_dwordx4 v[160:163], v[160:161], off
	s_mov_b64 s[18:19], 0x10000
	v_lshl_add_u64 v[164:165], v[130:131], 0, s[18:19]
	global_load_dwordx4 v[164:167], v[164:165], off offset:256
	s_mov_b64 s[18:19], 0x20000
	v_lshl_add_u64 v[168:169], v[130:131], 0, s[18:19]
	global_load_dwordx4 v[168:171], v[168:169], off
	s_mov_b64 s[18:19], 0x20000
	v_lshl_add_u64 v[172:173], v[130:131], 0, s[18:19]
	global_load_dwordx4 v[172:175], v[172:173], off offset:256
	s_mov_b64 s[18:19], 0x30000
	v_lshl_add_u64 v[176:177], v[130:131], 0, s[18:19]
	global_load_dwordx4 v[176:179], v[176:177], off
	s_mov_b64 s[18:19], 0x30000
	v_lshl_add_u64 v[180:181], v[130:131], 0, s[18:19]
	global_load_dwordx4 v[180:183], v[180:181], off offset:256
	s_mov_b64 s[18:19], 0x80000
	v_lshl_add_u64 v[184:185], v[130:131], 0, s[18:19]
	global_load_dwordx4 v[184:187], v[184:185], off
	s_mov_b64 s[18:19], 0x80000
	v_lshl_add_u64 v[188:189], v[130:131], 0, s[18:19]
	global_load_dwordx4 v[188:191], v[188:189], off offset:256
	s_mov_b64 s[18:19], 0x90000
	v_lshl_add_u64 v[192:193], v[130:131], 0, s[18:19]
	global_load_dwordx4 v[192:195], v[192:193], off
	s_mov_b64 s[18:19], 0x90000
	v_lshl_add_u64 v[196:197], v[130:131], 0, s[18:19]
	global_load_dwordx4 v[196:199], v[196:197], off offset:256
	s_mov_b64 s[18:19], 0xa0000
	v_lshl_add_u64 v[208:209], v[130:131], 0, s[18:19]
	global_load_dwordx4 v[208:211], v[208:209], off
	s_mov_b64 s[18:19], 0xa0000
	v_lshl_add_u64 v[212:213], v[130:131], 0, s[18:19]
	global_load_dwordx4 v[212:215], v[212:213], off offset:256
	s_mov_b64 s[18:19], 0xb0000
	v_lshl_add_u64 v[216:217], v[130:131], 0, s[18:19]
	global_load_dwordx4 v[216:219], v[216:217], off
	s_mov_b64 s[18:19], 0xb0000
	v_lshl_add_u64 v[220:221], v[130:131], 0, s[18:19]
	global_load_dwordx4 v[220:223], v[220:221], off offset:256
.Lwo_pf_done:
	s_andn2_b64 vcc, exec, s[16:17]
	v_lshl_add_u64 v[142:143], v[144:145], 2, s[14:15]
	s_cbranch_vccnz .LBB0_1311
	s_waitcnt vmcnt(14)
	v_pk_add_f32 v[132:133], v[128:129], v[154:155]
	v_pk_add_f32 v[130:131], v[126:127], v[152:153]
	v_pk_add_f32 v[136:137], v[124:125], v[158:159]
	v_pk_add_f32 v[134:135], v[122:123], v[156:157]
	s_cbranch_execz .LBB0_1312
	s_branch .LBB0_1315
.LBB0_1311:
.LBB0_1312:
	s_andn2_b64 vcc, exec, s[12:13]
	s_cbranch_vccnz .LBB0_1314
	s_waitcnt vmcnt(15)
	v_lshlrev_b32_e32 v134, 16, v152
	v_and_b32_e32 v135, 0xffff0000, v152
	v_lshlrev_b32_e32 v130, 16, v153
	v_and_b32_e32 v131, 0xffff0000, v153
	v_pk_add_f32 v[128:129], v[128:129], v[130:131]
	v_lshlrev_b32_e32 v130, 16, v154
	v_and_b32_e32 v131, 0xffff0000, v154
	v_lshlrev_b32_e32 v132, 16, v155
	v_and_b32_e32 v133, 0xffff0000, v155
	v_pk_add_f32 v[126:127], v[126:127], v[134:135]
	v_pk_add_f32 v[124:125], v[124:125], v[132:133]
	v_pk_add_f32 v[122:123], v[122:123], v[130:131]

; __device__ __forceinline__ unsigned cvt_pk_bf16(float lo, float hi) { unsigned r; asm volatile("v_cvt_pk_bf16_f32 %0, %1, %2" : "=v"(r) : "v"(lo), "v"(hi)); return r; }
;     __device__ __forceinline__ void operator()(const f32x4 (&acc)[2][2][4][2], const Unit& u, int wr, int wc, int fr, int fq) const {
;     ...
;             for (int m = 0; m < 4; ++m) { const size_t off = (size_t)(row0 + ai * HALF + m * 16) * ldc + col0; float sq_ = 0.f;
; #pragma unroll
;                 for (int bj = 0; bj < 2; ++bj) { f32x4 v0 = acc[ai][bj][m][0], v1 = acc[ai][bj][m][1];
;                     if (base32) { v0 += *(const f32x4*)(base32 + off + bj * HALF); v1 += *(const f32x4*)(base32 + off + bj * HALF + 4); }
;                     else if (base16) { const u32x4 b = *(const u32x4*)(base16 + off + bj * HALF);
;                         v0 += (f32x4){__uint_as_float(b.x << 16), __uint_as_float(b.x & 0xffff0000u), __uint_as_float(b.y << 16), __uint_as_float(b.y & 0xffff0000u)};
;                         v1 += (f32x4){__uint_as_float(b.z << 16), __uint_as_float(b.z & 0xffff0000u), __uint_as_float(b.w << 16), __uint_as_float(b.w & 0xffff0000u)}; }
;                     if (ssq) { float s_ = sq_; s_ = fmaf(v0[0], v0[0], s_); s_ = fmaf(v0[1], v0[1], s_); s_ = fmaf(v0[2], v0[2], s_); s_ = fmaf(v0[3], v0[3], s_);
;                       s_ = fmaf(v1[0], v1[0], s_); s_ = fmaf(v1[1], v1[1], s_); s_ = fmaf(v1[2], v1[2], s_); s_ = fmaf(v1[3], v1[3], s_); sq_ = s_; }
;                     u32x4 w; w.x = cvt_pk_bf16(v0[0], v0[1]); w.y = cvt_pk_bf16(v0[2], v0[3]); w.z = cvt_pk_bf16(v1[0], v1[1]); w.w = cvt_pk_bf16(v1[2], v1[3]);
;                     *(u32x4*)((u.kh ? out16b : out16) + off + bj * HALF) = w;
.LBB0_1315:
	v_cvt_pk_bf16_f32 v122, v130, v131
	v_lshl_add_u64 v[130:131], v[144:145], 1, s[0:1]
	s_and_b64 vcc, exec, s[42:43]
	v_cvt_pk_bf16_f32 v123, v132, v133
	v_cvt_pk_bf16_f32 v124, v134, v135
	v_cvt_pk_bf16_f32 v125, v136, v137
	global_store_dwordx4 v[130:131], v[122:125], off
	s_cbranch_vccnz .LBB0_1317
	s_waitcnt vmcnt(13)
	v_pk_add_f32 v[124:125], v[120:121], v[162:163]
	v_pk_add_f32 v[122:123], v[118:119], v[160:161]
	v_pk_add_f32 v[128:129], v[116:117], v[166:167]
	v_pk_add_f32 v[126:127], v[114:115], v[164:165]
	s_cbranch_execz .LBB0_1318
	s_branch .LBB0_1321
.LBB0_1317:
.LBB0_1318:
	s_andn2_b64 vcc, exec, s[12:13]
	s_cbranch_vccnz .LBB0_1320
	s_waitcnt vmcnt(15)
	v_lshlrev_b32_e32 v126, 16, v156
	v_and_b32_e32 v127, 0xffff0000, v156
	v_lshlrev_b32_e32 v122, 16, v157
	v_and_b32_e32 v123, 0xffff0000, v157
	v_pk_add_f32 v[120:121], v[120:121], v[122:123]
	v_lshlrev_b32_e32 v122, 16, v158
	v_and_b32_e32 v123, 0xffff0000, v158
	v_lshlrev_b32_e32 v124, 16, v159
	v_and_b32_e32 v125, 0xffff0000, v159
	v_pk_add_f32 v[118:119], v[118:119], v[126:127]
	v_pk_add_f32 v[116:117], v[116:117], v[124:125]
	v_pk_add_f32 v[114:115], v[114:115], v[122:123]

; __device__ __forceinline__ unsigned cvt_pk_bf16(float lo, float hi) { unsigned r; asm volatile("v_cvt_pk_bf16_f32 %0, %1, %2" : "=v"(r) : "v"(lo), "v"(hi)); return r; }
;     __device__ __forceinline__ void operator()(const f32x4 (&acc)[2][2][4][2], const Unit& u, int wr, int wc, int fr, int fq) const {
;     ...
;             for (int m = 0; m < 4; ++m) { const size_t off = (size_t)(row0 + ai * HALF + m * 16) * ldc + col0; float sq_ = 0.f;
; #pragma unroll
;                 for (int bj = 0; bj < 2; ++bj) { f32x4 v0 = acc[ai][bj][m][0], v1 = acc[ai][bj][m][1];
;                     if (base32) { v0 += *(const f32x4*)(base32 + off + bj * HALF); v1 += *(const f32x4*)(base32 + off + bj * HALF + 4); }
;                     else if (base16) { const u32x4 b = *(const u32x4*)(base16 + off + bj * HALF);
;                         v0 += (f32x4){__uint_as_float(b.x << 16), __uint_as_float(b.x & 0xffff0000u), __uint_as_float(b.y << 16), __uint_as_float(b.y & 0xffff0000u)};
;                         v1 += (f32x4){__uint_as_float(b.z << 16), __uint_as_float(b.z & 0xffff0000u), __uint_as_float(b.w << 16), __uint_as_float(b.w & 0xffff0000u)}; }
;                     if (ssq) { float s_ = sq_; s_ = fmaf(v0[0], v0[0], s_); s_ = fmaf(v0[1], v0[1], s_); s_ = fmaf(v0[2], v0[2], s_); s_ = fmaf(v0[3], v0[3], s_);
;                       s_ = fmaf(v1[0], v1[0], s_); s_ = fmaf(v1[1], v1[1], s_); s_ = fmaf(v1[2], v1[2], s_); s_ = fmaf(v1[3], v1[3], s_); sq_ = s_; }
;                     u32x4 w; w.x = cvt_pk_bf16(v0[0], v0[1]); w.y = cvt_pk_bf16(v0[2], v0[3]); w.z = cvt_pk_bf16(v1[0], v1[1]); w.w = cvt_pk_bf16(v1[2], v1[3]);
;                     *(u32x4*)((u.kh ? out16b : out16) + off + bj * HALF) = w;
.LBB0_1321:
	v_cvt_pk_bf16_f32 v114, v122, v123
	v_cvt_pk_bf16_f32 v115, v124, v125
	v_cvt_pk_bf16_f32 v116, v126, v127
	v_cvt_pk_bf16_f32 v117, v128, v129
	global_store_dwordx4 v[130:131], v[114:117], off offset:256
	s_and_b64 vcc, exec, s[42:43]
	s_nop 0
	v_or_b32_e32 v114, 16, v138
	v_ashrrev_i32_e32 v115, 31, v114
	v_lshlrev_b64 v[114:115], 11, v[114:115]
	v_lshl_add_u64 v[124:125], v[114:115], 0, v[140:141]
	v_lshl_add_u64 v[122:123], v[124:125], 2, s[14:15]
	s_cbranch_vccnz .LBB0_1323
	s_waitcnt vmcnt(12)
	v_pk_add_f32 v[116:117], v[112:113], v[170:171]
	v_pk_add_f32 v[114:115], v[110:111], v[168:169]
	v_pk_add_f32 v[120:121], v[108:109], v[174:175]
	v_pk_add_f32 v[118:119], v[106:107], v[172:173]
	s_cbranch_execz .LBB0_1324
	s_branch .LBB0_1327
.LBB0_1323:
.LBB0_1324:
	s_andn2_b64 vcc, exec, s[12:13]
	s_cbranch_vccnz .LBB0_1326
	s_waitcnt vmcnt(15)
	v_lshlrev_b32_e32 v118, 16, v160
	v_and_b32_e32 v119, 0xffff0000, v160
	v_lshlrev_b32_e32 v114, 16, v161
	v_and_b32_e32 v115, 0xffff0000, v161
	v_pk_add_f32 v[112:113], v[112:113], v[114:115]
	v_lshlrev_b32_e32 v114, 16, v162
	v_and_b32_e32 v115, 0xffff0000, v162
	v_lshlrev_b32_e32 v116, 16, v163
	v_and_b32_e32 v117, 0xffff0000, v163
	v_pk_add_f32 v[110:111], v[110:111], v[118:119]
	v_pk_add_f32 v[108:109], v[108:109], v[116:117]
	v_pk_add_f32 v[106:107], v[106:107], v[114:115]

; __device__ __forceinline__ unsigned cvt_pk_bf16(float lo, float hi) { unsigned r; asm volatile("v_cvt_pk_bf16_f32 %0, %1, %2" : "=v"(r) : "v"(lo), "v"(hi)); return r; }
;     __device__ __forceinline__ void operator()(const f32x4 (&acc)[2][2][4][2], const Unit& u, int wr, int wc, int fr, int fq) const {
;     ...
;             for (int m = 0; m < 4; ++m) { const size_t off = (size_t)(row0 + ai * HALF + m * 16) * ldc + col0; float sq_ = 0.f;
; #pragma unroll
;                 for (int bj = 0; bj < 2; ++bj) { f32x4 v0 = acc[ai][bj][m][0], v1 = acc[ai][bj][m][1];
;                     if (base32) { v0 += *(const f32x4*)(base32 + off + bj * HALF); v1 += *(const f32x4*)(base32 + off + bj * HALF + 4); }
;                     else if (base16) { const u32x4 b = *(const u32x4*)(base16 + off + bj * HALF);
;                         v0 += (f32x4){__uint_as_float(b.x << 16), __uint_as_float(b.x & 0xffff0000u), __uint_as_float(b.y << 16), __uint_as_float(b.y & 0xffff0000u)};
;                         v1 += (f32x4){__uint_as_float(b.z << 16), __uint_as_float(b.z & 0xffff0000u), __uint_as_float(b.w << 16), __uint_as_float(b.w & 0xffff0000u)}; }
;                     if (ssq) { float s_ = sq_; s_ = fmaf(v0[0], v0[0], s_); s_ = fmaf(v0[1], v0[1], s_); s_ = fmaf(v0[2], v0[2], s_); s_ = fmaf(v0[3], v0[3], s_);
;                       s_ = fmaf(v1[0], v1[0], s_); s_ = fmaf(v1[1], v1[1], s_); s_ = fmaf(v1[2], v1[2], s_); s_ = fmaf(v1[3], v1[3], s_); sq_ = s_; }
;                     u32x4 w; w.x = cvt_pk_bf16(v0[0], v0[1]); w.y = cvt_pk_bf16(v0[2], v0[3]); w.z = cvt_pk_bf16(v1[0], v1[1]); w.w = cvt_pk_bf16(v1[2], v1[3]);
;                     *(u32x4*)((u.kh ? out16b : out16) + off + bj * HALF) = w;
.LBB0_1327:
	v_cvt_pk_bf16_f32 v106, v114, v115
	v_lshl_add_u64 v[114:115], v[124:125], 1, s[0:1]
	s_and_b64 vcc, exec, s[42:43]
	v_cvt_pk_bf16_f32 v107, v116, v117
	v_cvt_pk_bf16_f32 v108, v118, v119
	v_cvt_pk_bf16_f32 v109, v120, v121
	global_store_dwordx4 v[114:115], v[106:109], off
	s_cbranch_vccnz .LBB0_1329
	s_waitcnt vmcnt(11)
	v_pk_add_f32 v[108:109], v[104:105], v[178:179]
	v_pk_add_f32 v[106:107], v[102:103], v[176:177]
	v_pk_add_f32 v[112:113], v[100:101], v[182:183]
	v_pk_add_f32 v[110:111], v[98:99], v[180:181]
	s_cbranch_execz .LBB0_1330
	s_branch .LBB0_1333
.LBB0_1329:
.LBB0_1330:
	s_andn2_b64 vcc, exec, s[12:13]
	s_cbranch_vccnz .LBB0_1332
	s_waitcnt vmcnt(15)
	v_lshlrev_b32_e32 v110, 16, v164
	v_and_b32_e32 v111, 0xffff0000, v164
	v_lshlrev_b32_e32 v106, 16, v165
	v_and_b32_e32 v107, 0xffff0000, v165
	v_pk_add_f32 v[104:105], v[104:105], v[106:107]
	v_lshlrev_b32_e32 v106, 16, v166
	v_and_b32_e32 v107, 0xffff0000, v166
	v_lshlrev_b32_e32 v108, 16, v167
	v_and_b32_e32 v109, 0xffff0000, v167
	v_pk_add_f32 v[102:103], v[102:103], v[110:111]
	v_pk_add_f32 v[100:101], v[100:101], v[108:109]
	v_pk_add_f32 v[98:99], v[98:99], v[106:107]

; __device__ __forceinline__ unsigned cvt_pk_bf16(float lo, float hi) { unsigned r; asm volatile("v_cvt_pk_bf16_f32 %0, %1, %2" : "=v"(r) : "v"(lo), "v"(hi)); return r; }
;     __device__ __forceinline__ void operator()(const f32x4 (&acc)[2][2][4][2], const Unit& u, int wr, int wc, int fr, int fq) const {
;     ...
;             for (int m = 0; m < 4; ++m) { const size_t off = (size_t)(row0 + ai * HALF + m * 16) * ldc + col0; float sq_ = 0.f;
; #pragma unroll
;                 for (int bj = 0; bj < 2; ++bj) { f32x4 v0 = acc[ai][bj][m][0], v1 = acc[ai][bj][m][1];
;                     if (base32) { v0 += *(const f32x4*)(base32 + off + bj * HALF); v1 += *(const f32x4*)(base32 + off + bj * HALF + 4); }
;                     else if (base16) { const u32x4 b = *(const u32x4*)(base16 + off + bj * HALF);
;                         v0 += (f32x4){__uint_as_float(b.x << 16), __uint_as_float(b.x & 0xffff0000u), __uint_as_float(b.y << 16), __uint_as_float(b.y & 0xffff0000u)};
;                         v1 += (f32x4){__uint_as_float(b.z << 16), __uint_as_float(b.z & 0xffff0000u), __uint_as_float(b.w << 16), __uint_as_float(b.w & 0xffff0000u)}; }
;                     if (ssq) { float s_ = sq_; s_ = fmaf(v0[0], v0[0], s_); s_ = fmaf(v0[1], v0[1], s_); s_ = fmaf(v0[2], v0[2], s_); s_ = fmaf(v0[3], v0[3], s_);
;                       s_ = fmaf(v1[0], v1[0], s_); s_ = fmaf(v1[1], v1[1], s_); s_ = fmaf(v1[2], v1[2], s_); s_ = fmaf(v1[3], v1[3], s_); sq_ = s_; }
;                     u32x4 w; w.x = cvt_pk_bf16(v0[0], v0[1]); w.y = cvt_pk_bf16(v0[2], v0[3]); w.z = cvt_pk_bf16(v1[0], v1[1]); w.w = cvt_pk_bf16(v1[2], v1[3]);
;                     *(u32x4*)((u.kh ? out16b : out16) + off + bj * HALF) = w;
.LBB0_1333:
	v_cvt_pk_bf16_f32 v98, v106, v107
	v_cvt_pk_bf16_f32 v99, v108, v109
	v_cvt_pk_bf16_f32 v100, v110, v111
	v_cvt_pk_bf16_f32 v101, v112, v113
	global_store_dwordx4 v[114:115], v[98:101], off offset:256
	s_and_b64 vcc, exec, s[42:43]
	s_nop 0
	v_or_b32_e32 v98, 32, v138
	v_ashrrev_i32_e32 v99, 31, v98
	v_lshlrev_b64 v[98:99], 11, v[98:99]
	v_lshl_add_u64 v[108:109], v[98:99], 0, v[140:141]
	v_lshl_add_u64 v[106:107], v[108:109], 2, s[14:15]
	s_cbranch_vccnz .LBB0_1335
	s_waitcnt vmcnt(10)
	v_pk_add_f32 v[100:101], v[96:97], v[186:187]
	v_pk_add_f32 v[98:99], v[94:95], v[184:185]
	v_pk_add_f32 v[104:105], v[92:93], v[190:191]
	v_pk_add_f32 v[102:103], v[90:91], v[188:189]
	s_cbranch_execz .LBB0_1336
	s_branch .LBB0_1339
.LBB0_1335:
.LBB0_1336:
	s_andn2_b64 vcc, exec, s[12:13]
	s_cbranch_vccnz .LBB0_1338
	s_waitcnt vmcnt(15)
	v_lshlrev_b32_e32 v102, 16, v168
	v_and_b32_e32 v103, 0xffff0000, v168
	v_lshlrev_b32_e32 v98, 16, v169
	v_and_b32_e32 v99, 0xffff0000, v169
	v_pk_add_f32 v[96:97], v[96:97], v[98:99]
	v_lshlrev_b32_e32 v98, 16, v170
	v_and_b32_e32 v99, 0xffff0000, v170
	v_lshlrev_b32_e32 v100, 16, v171
	v_and_b32_e32 v101, 0xffff0000, v171
	v_pk_add_f32 v[94:95], v[94:95], v[102:103]
	v_pk_add_f32 v[92:93], v[92:93], v[100:101]
	v_pk_add_f32 v[90:91], v[90:91], v[98:99]

; __device__ __forceinline__ unsigned cvt_pk_bf16(float lo, float hi) { unsigned r; asm volatile("v_cvt_pk_bf16_f32 %0, %1, %2" : "=v"(r) : "v"(lo), "v"(hi)); return r; }
;     __device__ __forceinline__ void operator()(const f32x4 (&acc)[2][2][4][2], const Unit& u, int wr, int wc, int fr, int fq) const {
;     ...
;             for (int m = 0; m < 4; ++m) { const size_t off = (size_t)(row0 + ai * HALF + m * 16) * ldc + col0; float sq_ = 0.f;
; #pragma unroll
;                 for (int bj = 0; bj < 2; ++bj) { f32x4 v0 = acc[ai][bj][m][0], v1 = acc[ai][bj][m][1];
;                     if (base32) { v0 += *(const f32x4*)(base32 + off + bj * HALF); v1 += *(const f32x4*)(base32 + off + bj * HALF + 4); }
;                     else if (base16) { const u32x4 b = *(const u32x4*)(base16 + off + bj * HALF);
;                         v0 += (f32x4){__uint_as_float(b.x << 16), __uint_as_float(b.x & 0xffff0000u), __uint_as_float(b.y << 16), __uint_as_float(b.y & 0xffff0000u)};
;                         v1 += (f32x4){__uint_as_float(b.z << 16), __uint_as_float(b.z & 0xffff0000u), __uint_as_float(b.w << 16), __uint_as_float(b.w & 0xffff0000u)}; }
;                     if (ssq) { float s_ = sq_; s_ = fmaf(v0[0], v0[0], s_); s_ = fmaf(v0[1], v0[1], s_); s_ = fmaf(v0[2], v0[2], s_); s_ = fmaf(v0[3], v0[3], s_);
;                       s_ = fmaf(v1[0], v1[0], s_); s_ = fmaf(v1[1], v1[1], s_); s_ = fmaf(v1[2], v1[2], s_); s_ = fmaf(v1[3], v1[3], s_); sq_ = s_; }
;                     u32x4 w; w.x = cvt_pk_bf16(v0[0], v0[1]); w.y = cvt_pk_bf16(v0[2], v0[3]); w.z = cvt_pk_bf16(v1[0], v1[1]); w.w = cvt_pk_bf16(v1[2], v1[3]);
;                     *(u32x4*)((u.kh ? out16b : out16) + off + bj * HALF) = w;
.LBB0_1339:
	v_cvt_pk_bf16_f32 v90, v98, v99
	v_lshl_add_u64 v[98:99], v[108:109], 1, s[0:1]
	s_and_b64 vcc, exec, s[42:43]
	v_cvt_pk_bf16_f32 v91, v100, v101
	v_cvt_pk_bf16_f32 v92, v102, v103
	v_cvt_pk_bf16_f32 v93, v104, v105
	global_store_dwordx4 v[98:99], v[90:93], off
	s_cbranch_vccnz .LBB0_1341
	s_waitcnt vmcnt(9)
	v_pk_add_f32 v[92:93], v[88:89], v[194:195]
	v_pk_add_f32 v[90:91], v[86:87], v[192:193]
	v_pk_add_f32 v[96:97], v[84:85], v[198:199]
	v_pk_add_f32 v[94:95], v[82:83], v[196:197]
	s_cbranch_execz .LBB0_1342
	s_branch .LBB0_1345
.LBB0_1341:
.LBB0_1342:
	s_andn2_b64 vcc, exec, s[12:13]
	s_cbranch_vccnz .LBB0_1344
	s_waitcnt vmcnt(15)
	v_lshlrev_b32_e32 v94, 16, v172
	v_and_b32_e32 v95, 0xffff0000, v172
	v_lshlrev_b32_e32 v90, 16, v173
	v_and_b32_e32 v91, 0xffff0000, v173
	v_pk_add_f32 v[88:89], v[88:89], v[90:91]
	v_lshlrev_b32_e32 v90, 16, v174
	v_and_b32_e32 v91, 0xffff0000, v174
	v_lshlrev_b32_e32 v92, 16, v175
	v_and_b32_e32 v93, 0xffff0000, v175
	v_pk_add_f32 v[86:87], v[86:87], v[94:95]
	v_pk_add_f32 v[84:85], v[84:85], v[92:93]
	v_pk_add_f32 v[82:83], v[82:83], v[90:91]

; __device__ __forceinline__ unsigned cvt_pk_bf16(float lo, float hi) { unsigned r; asm volatile("v_cvt_pk_bf16_f32 %0, %1, %2" : "=v"(r) : "v"(lo), "v"(hi)); return r; }
;     __device__ __forceinline__ void operator()(const f32x4 (&acc)[2][2][4][2], const Unit& u, int wr, int wc, int fr, int fq) const {
;     ...
;             for (int m = 0; m < 4; ++m) { const size_t off = (size_t)(row0 + ai * HALF + m * 16) * ldc + col0; float sq_ = 0.f;
; #pragma unroll
;                 for (int bj = 0; bj < 2; ++bj) { f32x4 v0 = acc[ai][bj][m][0], v1 = acc[ai][bj][m][1];
;                     if (base32) { v0 += *(const f32x4*)(base32 + off + bj * HALF); v1 += *(const f32x4*)(base32 + off + bj * HALF + 4); }
;                     else if (base16) { const u32x4 b = *(const u32x4*)(base16 + off + bj * HALF);
;                         v0 += (f32x4){__uint_as_float(b.x << 16), __uint_as_float(b.x & 0xffff0000u), __uint_as_float(b.y << 16), __uint_as_float(b.y & 0xffff0000u)};
;                         v1 += (f32x4){__uint_as_float(b.z << 16), __uint_as_float(b.z & 0xffff0000u), __uint_as_float(b.w << 16), __uint_as_float(b.w & 0xffff0000u)}; }
;                     if (ssq) { float s_ = sq_; s_ = fmaf(v0[0], v0[0], s_); s_ = fmaf(v0[1], v0[1], s_); s_ = fmaf(v0[2], v0[2], s_); s_ = fmaf(v0[3], v0[3], s_);
;                       s_ = fmaf(v1[0], v1[0], s_); s_ = fmaf(v1[1], v1[1], s_); s_ = fmaf(v1[2], v1[2], s_); s_ = fmaf(v1[3], v1[3], s_); sq_ = s_; }
;                     u32x4 w; w.x = cvt_pk_bf16(v0[0], v0[1]); w.y = cvt_pk_bf16(v0[2], v0[3]); w.z = cvt_pk_bf16(v1[0], v1[1]); w.w = cvt_pk_bf16(v1[2], v1[3]);
;                     *(u32x4*)((u.kh ? out16b : out16) + off + bj * HALF) = w;
.LBB0_1345:
	v_cvt_pk_bf16_f32 v82, v90, v91
	v_cvt_pk_bf16_f32 v83, v92, v93
	v_cvt_pk_bf16_f32 v84, v94, v95
	v_cvt_pk_bf16_f32 v85, v96, v97
	global_store_dwordx4 v[98:99], v[82:85], off offset:256
	s_and_b64 vcc, exec, s[42:43]
	s_nop 0
	v_or_b32_e32 v82, 48, v138
	v_ashrrev_i32_e32 v83, 31, v82
	v_lshlrev_b64 v[82:83], 11, v[82:83]
	v_lshl_add_u64 v[92:93], v[82:83], 0, v[140:141]
	v_lshl_add_u64 v[90:91], v[92:93], 2, s[14:15]
	s_cbranch_vccnz .LBB0_1347
	s_waitcnt vmcnt(8)
	v_pk_add_f32 v[84:85], v[80:81], v[210:211]
	v_pk_add_f32 v[82:83], v[78:79], v[208:209]
	v_pk_add_f32 v[88:89], v[76:77], v[214:215]
	v_pk_add_f32 v[86:87], v[74:75], v[212:213]
	s_cbranch_execz .LBB0_1348
	s_branch .LBB0_1351
.LBB0_1347:
.LBB0_1348:
	s_andn2_b64 vcc, exec, s[12:13]
	s_cbranch_vccnz .LBB0_1350
	s_waitcnt vmcnt(15)
	v_lshlrev_b32_e32 v86, 16, v176
	v_and_b32_e32 v87, 0xffff0000, v176
	v_lshlrev_b32_e32 v82, 16, v177
	v_and_b32_e32 v83, 0xffff0000, v177
	v_pk_add_f32 v[80:81], v[80:81], v[82:83]
	v_lshlrev_b32_e32 v82, 16, v178
	v_and_b32_e32 v83, 0xffff0000, v178
	v_lshlrev_b32_e32 v84, 16, v179
	v_and_b32_e32 v85, 0xffff0000, v179
	v_pk_add_f32 v[78:79], v[78:79], v[86:87]
	v_pk_add_f32 v[76:77], v[76:77], v[84:85]
	v_pk_add_f32 v[74:75], v[74:75], v[82:83]

; __device__ __forceinline__ unsigned cvt_pk_bf16(float lo, float hi) { unsigned r; asm volatile("v_cvt_pk_bf16_f32 %0, %1, %2" : "=v"(r) : "v"(lo), "v"(hi)); return r; }
;     __device__ __forceinline__ void operator()(const f32x4 (&acc)[2][2][4][2], const Unit& u, int wr, int wc, int fr, int fq) const {
;     ...
;             for (int m = 0; m < 4; ++m) { const size_t off = (size_t)(row0 + ai * HALF + m * 16) * ldc + col0; float sq_ = 0.f;
; #pragma unroll
;                 for (int bj = 0; bj < 2; ++bj) { f32x4 v0 = acc[ai][bj][m][0], v1 = acc[ai][bj][m][1];
;                     if (base32) { v0 += *(const f32x4*)(base32 + off + bj * HALF); v1 += *(const f32x4*)(base32 + off + bj * HALF + 4); }
;                     else if (base16) { const u32x4 b = *(const u32x4*)(base16 + off + bj * HALF);
;                         v0 += (f32x4){__uint_as_float(b.x << 16), __uint_as_float(b.x & 0xffff0000u), __uint_as_float(b.y << 16), __uint_as_float(b.y & 0xffff0000u)};
;                         v1 += (f32x4){__uint_as_float(b.z << 16), __uint_as_float(b.z & 0xffff0000u), __uint_as_float(b.w << 16), __uint_as_float(b.w & 0xffff0000u)}; }
;                     if (ssq) { float s_ = sq_; s_ = fmaf(v0[0], v0[0], s_); s_ = fmaf(v0[1], v0[1], s_); s_ = fmaf(v0[2], v0[2], s_); s_ = fmaf(v0[3], v0[3], s_);
;                       s_ = fmaf(v1[0], v1[0], s_); s_ = fmaf(v1[1], v1[1], s_); s_ = fmaf(v1[2], v1[2], s_); s_ = fmaf(v1[3], v1[3], s_); sq_ = s_; }
;                     u32x4 w; w.x = cvt_pk_bf16(v0[0], v0[1]); w.y = cvt_pk_bf16(v0[2], v0[3]); w.z = cvt_pk_bf16(v1[0], v1[1]); w.w = cvt_pk_bf16(v1[2], v1[3]);
;                     *(u32x4*)((u.kh ? out16b : out16) + off + bj * HALF) = w;
.LBB0_1351:
	v_cvt_pk_bf16_f32 v74, v82, v83
	v_lshl_add_u64 v[82:83], v[92:93], 1, s[0:1]
	s_and_b64 vcc, exec, s[42:43]
	v_cvt_pk_bf16_f32 v75, v84, v85
	v_cvt_pk_bf16_f32 v76, v86, v87
	v_cvt_pk_bf16_f32 v77, v88, v89
	global_store_dwordx4 v[82:83], v[74:77], off
	s_cbranch_vccnz .LBB0_1353
	s_waitcnt vmcnt(7)
	v_pk_add_f32 v[76:77], v[72:73], v[218:219]
	v_pk_add_f32 v[74:75], v[70:71], v[216:217]
	v_pk_add_f32 v[80:81], v[68:69], v[222:223]
	v_pk_add_f32 v[78:79], v[66:67], v[220:221]
	s_cbranch_execz .LBB0_1354
	s_branch .LBB0_1357
.LBB0_1353:
.LBB0_1354:
	s_andn2_b64 vcc, exec, s[12:13]
	s_cbranch_vccnz .LBB0_1356
	s_waitcnt vmcnt(15)
	v_lshlrev_b32_e32 v78, 16, v180
	v_and_b32_e32 v79, 0xffff0000, v180
	v_lshlrev_b32_e32 v74, 16, v181
	v_and_b32_e32 v75, 0xffff0000, v181
	v_pk_add_f32 v[72:73], v[72:73], v[74:75]
	v_lshlrev_b32_e32 v74, 16, v182
	v_and_b32_e32 v75, 0xffff0000, v182
	v_lshlrev_b32_e32 v76, 16, v183
	v_and_b32_e32 v77, 0xffff0000, v183
	v_pk_add_f32 v[70:71], v[70:71], v[78:79]
	v_pk_add_f32 v[68:69], v[68:69], v[76:77]
	v_pk_add_f32 v[66:67], v[66:67], v[74:75]

; __device__ __forceinline__ unsigned cvt_pk_bf16(float lo, float hi) { unsigned r; asm volatile("v_cvt_pk_bf16_f32 %0, %1, %2" : "=v"(r) : "v"(lo), "v"(hi)); return r; }
;     __device__ __forceinline__ void operator()(const f32x4 (&acc)[2][2][4][2], const Unit& u, int wr, int wc, int fr, int fq) const {
;     ...
;             for (int m = 0; m < 4; ++m) { const size_t off = (size_t)(row0 + ai * HALF + m * 16) * ldc + col0; float sq_ = 0.f;
; #pragma unroll
;                 for (int bj = 0; bj < 2; ++bj) { f32x4 v0 = acc[ai][bj][m][0], v1 = acc[ai][bj][m][1];
;                     if (base32) { v0 += *(const f32x4*)(base32 + off + bj * HALF); v1 += *(const f32x4*)(base32 + off + bj * HALF + 4); }
;                     else if (base16) { const u32x4 b = *(const u32x4*)(base16 + off + bj * HALF);
;                         v0 += (f32x4){__uint_as_float(b.x << 16), __uint_as_float(b.x & 0xffff0000u), __uint_as_float(b.y << 16), __uint_as_float(b.y & 0xffff0000u)};
;                         v1 += (f32x4){__uint_as_float(b.z << 16), __uint_as_float(b.z & 0xffff0000u), __uint_as_float(b.w << 16), __uint_as_float(b.w & 0xffff0000u)}; }
;                     if (ssq) { float s_ = sq_; s_ = fmaf(v0[0], v0[0], s_); s_ = fmaf(v0[1], v0[1], s_); s_ = fmaf(v0[2], v0[2], s_); s_ = fmaf(v0[3], v0[3], s_);
;                       s_ = fmaf(v1[0], v1[0], s_); s_ = fmaf(v1[1], v1[1], s_); s_ = fmaf(v1[2], v1[2], s_); s_ = fmaf(v1[3], v1[3], s_); sq_ = s_; }
;                     u32x4 w; w.x = cvt_pk_bf16(v0[0], v0[1]); w.y = cvt_pk_bf16(v0[2], v0[3]); w.z = cvt_pk_bf16(v1[0], v1[1]); w.w = cvt_pk_bf16(v1[2], v1[3]);
;                     *(u32x4*)((u.kh ? out16b : out16) + off + bj * HALF) = w;
.LBB0_1357:
	v_cvt_pk_bf16_f32 v66, v74, v75
	v_cvt_pk_bf16_f32 v67, v76, v77
	v_cvt_pk_bf16_f32 v68, v78, v79
	v_cvt_pk_bf16_f32 v69, v80, v81
	global_store_dwordx4 v[82:83], v[66:69], off offset:256
	s_mov_b64 s[18:19], 0x40000
	s_and_b64 vcc, exec, s[42:43]
	v_lshlrev_b64 v[66:67], 11, v[138:139]
	v_lshl_add_u64 v[66:67], v[66:67], 0, v[140:141]
	v_lshl_add_u64 v[76:77], v[66:67], 0, s[18:19]
	v_lshl_add_u64 v[74:75], v[76:77], 2, s[14:15]
	s_cbranch_vccnz .LBB0_1359
	s_mov_b64 s[18:19], 0x100000
	v_lshl_add_u64 v[152:153], v[142:143], 0, s[18:19]
	global_load_dwordx4 v[156:159], v[152:153], off offset:16
	global_load_dwordx4 v[152:155], v[152:153], off
	s_mov_b64 s[18:19], 0x100000
	v_lshl_add_u64 v[160:161], v[142:143], 0, s[18:19]
	global_load_dwordx4 v[164:167], v[160:161], off offset:528
	global_load_dwordx4 v[160:163], v[160:161], off offset:512
	s_mov_b64 s[18:19], 0x120000
	v_lshl_add_u64 v[168:169], v[142:143], 0, s[18:19]
	global_load_dwordx4 v[172:175], v[168:169], off offset:16
	global_load_dwordx4 v[168:171], v[168:169], off
	s_mov_b64 s[18:19], 0x120000
	v_lshl_add_u64 v[176:177], v[142:143], 0, s[18:19]
	global_load_dwordx4 v[180:183], v[176:177], off offset:528
	global_load_dwordx4 v[176:179], v[176:177], off offset:512
	s_mov_b64 s[18:19], 0x140000
	v_lshl_add_u64 v[184:185], v[142:143], 0, s[18:19]
	global_load_dwordx4 v[188:191], v[184:185], off offset:16
	global_load_dwordx4 v[184:187], v[184:185], off
	s_mov_b64 s[18:19], 0x140000
	v_lshl_add_u64 v[192:193], v[142:143], 0, s[18:19]
	global_load_dwordx4 v[196:199], v[192:193], off offset:528
	global_load_dwordx4 v[192:195], v[192:193], off offset:512
	s_mov_b64 s[18:19], 0x160000
	v_lshl_add_u64 v[208:209], v[142:143], 0, s[18:19]
	global_load_dwordx4 v[212:215], v[208:209], off offset:16
	global_load_dwordx4 v[208:211], v[208:209], off
	s_mov_b64 s[18:19], 0x160000
	v_lshl_add_u64 v[216:217], v[142:143], 0, s[18:19]
	global_load_dwordx4 v[220:223], v[216:217], off offset:528
	global_load_dwordx4 v[216:219], v[216:217], off offset:512
	s_waitcnt vmcnt(14)
	v_pk_add_f32 v[68:69], v[64:65], v[154:155]
	v_pk_add_f32 v[66:67], v[62:63], v[152:153]
	v_pk_add_f32 v[72:73], v[60:61], v[158:159]
	v_pk_add_f32 v[70:71], v[58:59], v[156:157]
	s_cbranch_execz .LBB0_1360
	s_branch .LBB0_1363
.LBB0_1359:
.LBB0_1360:
	s_andn2_b64 vcc, exec, s[12:13]
	s_cbranch_vccnz .LBB0_1362
	s_waitcnt vmcnt(15)
	v_lshlrev_b32_e32 v70, 16, v184
	v_and_b32_e32 v71, 0xffff0000, v184
	v_lshlrev_b32_e32 v66, 16, v185
	v_and_b32_e32 v67, 0xffff0000, v185
	v_pk_add_f32 v[64:65], v[64:65], v[66:67]
	v_lshlrev_b32_e32 v66, 16, v186
	v_and_b32_e32 v67, 0xffff0000, v186
	v_lshlrev_b32_e32 v68, 16, v187
	v_and_b32_e32 v69, 0xffff0000, v187
	v_pk_add_f32 v[62:63], v[62:63], v[70:71]
	v_pk_add_f32 v[60:61], v[60:61], v[68:69]
	v_pk_add_f32 v[58:59], v[58:59], v[66:67]

; __device__ __forceinline__ unsigned cvt_pk_bf16(float lo, float hi) { unsigned r; asm volatile("v_cvt_pk_bf16_f32 %0, %1, %2" : "=v"(r) : "v"(lo), "v"(hi)); return r; }
;     __device__ __forceinline__ void operator()(const f32x4 (&acc)[2][2][4][2], const Unit& u, int wr, int wc, int fr, int fq) const {
;     ...
;             for (int m = 0; m < 4; ++m) { const size_t off = (size_t)(row0 + ai * HALF + m * 16) * ldc + col0; float sq_ = 0.f;
; #pragma unroll
;                 for (int bj = 0; bj < 2; ++bj) { f32x4 v0 = acc[ai][bj][m][0], v1 = acc[ai][bj][m][1];
;                     if (base32) { v0 += *(const f32x4*)(base32 + off + bj * HALF); v1 += *(const f32x4*)(base32 + off + bj * HALF + 4); }
;                     else if (base16) { const u32x4 b = *(const u32x4*)(base16 + off + bj * HALF);
;                         v0 += (f32x4){__uint_as_float(b.x << 16), __uint_as_float(b.x & 0xffff0000u), __uint_as_float(b.y << 16), __uint_as_float(b.y & 0xffff0000u)};
;                         v1 += (f32x4){__uint_as_float(b.z << 16), __uint_as_float(b.z & 0xffff0000u), __uint_as_float(b.w << 16), __uint_as_float(b.w & 0xffff0000u)}; }
;                     if (ssq) { float s_ = sq_; s_ = fmaf(v0[0], v0[0], s_); s_ = fmaf(v0[1], v0[1], s_); s_ = fmaf(v0[2], v0[2], s_); s_ = fmaf(v0[3], v0[3], s_);
;                       s_ = fmaf(v1[0], v1[0], s_); s_ = fmaf(v1[1], v1[1], s_); s_ = fmaf(v1[2], v1[2], s_); s_ = fmaf(v1[3], v1[3], s_); sq_ = s_; }
;                     u32x4 w; w.x = cvt_pk_bf16(v0[0], v0[1]); w.y = cvt_pk_bf16(v0[2], v0[3]); w.z = cvt_pk_bf16(v1[0], v1[1]); w.w = cvt_pk_bf16(v1[2], v1[3]);
;                     *(u32x4*)((u.kh ? out16b : out16) + off + bj * HALF) = w;
.LBB0_1363:
	v_cvt_pk_bf16_f32 v58, v66, v67
	v_lshl_add_u64 v[66:67], v[76:77], 1, s[0:1]
	s_and_b64 vcc, exec, s[42:43]
	v_cvt_pk_bf16_f32 v59, v68, v69
	v_cvt_pk_bf16_f32 v60, v70, v71
	v_cvt_pk_bf16_f32 v61, v72, v73
	global_store_dwordx4 v[66:67], v[58:61], off
	s_cbranch_vccnz .LBB0_1365
	s_waitcnt vmcnt(13)
	v_pk_add_f32 v[60:61], v[56:57], v[162:163]
	v_pk_add_f32 v[58:59], v[54:55], v[160:161]
	v_pk_add_f32 v[64:65], v[52:53], v[166:167]
	v_pk_add_f32 v[62:63], v[50:51], v[164:165]
	s_cbranch_execz .LBB0_1366
	s_branch .LBB0_1369
.LBB0_1365:
.LBB0_1366:
	s_andn2_b64 vcc, exec, s[12:13]
	s_cbranch_vccnz .LBB0_1368
	s_waitcnt vmcnt(15)
	v_lshlrev_b32_e32 v62, 16, v188
	v_and_b32_e32 v63, 0xffff0000, v188
	v_lshlrev_b32_e32 v58, 16, v189
	v_and_b32_e32 v59, 0xffff0000, v189
	v_pk_add_f32 v[56:57], v[56:57], v[58:59]
	v_lshlrev_b32_e32 v58, 16, v190
	v_and_b32_e32 v59, 0xffff0000, v190
	v_lshlrev_b32_e32 v60, 16, v191
	v_and_b32_e32 v61, 0xffff0000, v191
	v_pk_add_f32 v[54:55], v[54:55], v[62:63]
	v_pk_add_f32 v[52:53], v[52:53], v[60:61]
	v_pk_add_f32 v[50:51], v[50:51], v[58:59]

; __device__ __forceinline__ unsigned cvt_pk_bf16(float lo, float hi) { unsigned r; asm volatile("v_cvt_pk_bf16_f32 %0, %1, %2" : "=v"(r) : "v"(lo), "v"(hi)); return r; }
;     __device__ __forceinline__ void operator()(const f32x4 (&acc)[2][2][4][2], const Unit& u, int wr, int wc, int fr, int fq) const {
;     ...
;             for (int m = 0; m < 4; ++m) { const size_t off = (size_t)(row0 + ai * HALF + m * 16) * ldc + col0; float sq_ = 0.f;
; #pragma unroll
;                 for (int bj = 0; bj < 2; ++bj) { f32x4 v0 = acc[ai][bj][m][0], v1 = acc[ai][bj][m][1];
;                     if (base32) { v0 += *(const f32x4*)(base32 + off + bj * HALF); v1 += *(const f32x4*)(base32 + off + bj * HALF + 4); }
;                     else if (base16) { const u32x4 b = *(const u32x4*)(base16 + off + bj * HALF);
;                         v0 += (f32x4){__uint_as_float(b.x << 16), __uint_as_float(b.x & 0xffff0000u), __uint_as_float(b.y << 16), __uint_as_float(b.y & 0xffff0000u)};
;                         v1 += (f32x4){__uint_as_float(b.z << 16), __uint_as_float(b.z & 0xffff0000u), __uint_as_float(b.w << 16), __uint_as_float(b.w & 0xffff0000u)}; }
;                     if (ssq) { float s_ = sq_; s_ = fmaf(v0[0], v0[0], s_); s_ = fmaf(v0[1], v0[1], s_); s_ = fmaf(v0[2], v0[2], s_); s_ = fmaf(v0[3], v0[3], s_);
;                       s_ = fmaf(v1[0], v1[0], s_); s_ = fmaf(v1[1], v1[1], s_); s_ = fmaf(v1[2], v1[2], s_); s_ = fmaf(v1[3], v1[3], s_); sq_ = s_; }
;                     u32x4 w; w.x = cvt_pk_bf16(v0[0], v0[1]); w.y = cvt_pk_bf16(v0[2], v0[3]); w.z = cvt_pk_bf16(v1[0], v1[1]); w.w = cvt_pk_bf16(v1[2], v1[3]);
;                     *(u32x4*)((u.kh ? out16b : out16) + off + bj * HALF) = w;
.LBB0_1369:
	v_cvt_pk_bf16_f32 v50, v58, v59
	v_cvt_pk_bf16_f32 v51, v60, v61
	v_cvt_pk_bf16_f32 v52, v62, v63
	v_cvt_pk_bf16_f32 v53, v64, v65
	global_store_dwordx4 v[66:67], v[50:53], off offset:256
	s_mov_b64 s[18:19], 0x48000
	s_and_b64 vcc, exec, s[42:43]
	v_lshlrev_b64 v[50:51], 11, v[138:139]
	v_lshl_add_u64 v[50:51], v[50:51], 0, v[140:141]
	v_lshl_add_u64 v[60:61], v[50:51], 0, s[18:19]
	v_lshl_add_u64 v[58:59], v[60:61], 2, s[14:15]
	s_cbranch_vccnz .LBB0_1371
	s_waitcnt vmcnt(12)
	v_pk_add_f32 v[52:53], v[48:49], v[170:171]
	v_pk_add_f32 v[50:51], v[46:47], v[168:169]
	v_pk_add_f32 v[56:57], v[44:45], v[174:175]
	v_pk_add_f32 v[54:55], v[42:43], v[172:173]
	s_cbranch_execz .LBB0_1372
	s_branch .LBB0_1375
.LBB0_1371:
.LBB0_1372:
	s_andn2_b64 vcc, exec, s[12:13]
	s_cbranch_vccnz .LBB0_1374
	s_waitcnt vmcnt(15)
	v_lshlrev_b32_e32 v54, 16, v192
	v_and_b32_e32 v55, 0xffff0000, v192
	v_lshlrev_b32_e32 v50, 16, v193
	v_and_b32_e32 v51, 0xffff0000, v193
	v_pk_add_f32 v[48:49], v[48:49], v[50:51]
	v_lshlrev_b32_e32 v50, 16, v194
	v_and_b32_e32 v51, 0xffff0000, v194
	v_lshlrev_b32_e32 v52, 16, v195
	v_and_b32_e32 v53, 0xffff0000, v195
	v_pk_add_f32 v[46:47], v[46:47], v[54:55]
	v_pk_add_f32 v[44:45], v[44:45], v[52:53]
	v_pk_add_f32 v[42:43], v[42:43], v[50:51]

; __device__ __forceinline__ unsigned cvt_pk_bf16(float lo, float hi) { unsigned r; asm volatile("v_cvt_pk_bf16_f32 %0, %1, %2" : "=v"(r) : "v"(lo), "v"(hi)); return r; }
;     __device__ __forceinline__ void operator()(const f32x4 (&acc)[2][2][4][2], const Unit& u, int wr, int wc, int fr, int fq) const {
;     ...
;             for (int m = 0; m < 4; ++m) { const size_t off = (size_t)(row0 + ai * HALF + m * 16) * ldc + col0; float sq_ = 0.f;
; #pragma unroll
;                 for (int bj = 0; bj < 2; ++bj) { f32x4 v0 = acc[ai][bj][m][0], v1 = acc[ai][bj][m][1];
;                     if (base32) { v0 += *(const f32x4*)(base32 + off + bj * HALF); v1 += *(const f32x4*)(base32 + off + bj * HALF + 4); }
;                     else if (base16) { const u32x4 b = *(const u32x4*)(base16 + off + bj * HALF);
;                         v0 += (f32x4){__uint_as_float(b.x << 16), __uint_as_float(b.x & 0xffff0000u), __uint_as_float(b.y << 16), __uint_as_float(b.y & 0xffff0000u)};
;                         v1 += (f32x4){__uint_as_float(b.z << 16), __uint_as_float(b.z & 0xffff0000u), __uint_as_float(b.w << 16), __uint_as_float(b.w & 0xffff0000u)}; }
;                     if (ssq) { float s_ = sq_; s_ = fmaf(v0[0], v0[0], s_); s_ = fmaf(v0[1], v0[1], s_); s_ = fmaf(v0[2], v0[2], s_); s_ = fmaf(v0[3], v0[3], s_);
;                       s_ = fmaf(v1[0], v1[0], s_); s_ = fmaf(v1[1], v1[1], s_); s_ = fmaf(v1[2], v1[2], s_); s_ = fmaf(v1[3], v1[3], s_); sq_ = s_; }
;                     u32x4 w; w.x = cvt_pk_bf16(v0[0], v0[1]); w.y = cvt_pk_bf16(v0[2], v0[3]); w.z = cvt_pk_bf16(v1[0], v1[1]); w.w = cvt_pk_bf16(v1[2], v1[3]);
;                     *(u32x4*)((u.kh ? out16b : out16) + off + bj * HALF) = w;
.LBB0_1375:
	v_cvt_pk_bf16_f32 v42, v50, v51
	v_lshl_add_u64 v[50:51], v[60:61], 1, s[0:1]
	s_and_b64 vcc, exec, s[42:43]
	v_cvt_pk_bf16_f32 v43, v52, v53
	v_cvt_pk_bf16_f32 v44, v54, v55
	v_cvt_pk_bf16_f32 v45, v56, v57
	global_store_dwordx4 v[50:51], v[42:45], off
	s_cbranch_vccnz .LBB0_1377
	s_waitcnt vmcnt(11)
	v_pk_add_f32 v[44:45], v[40:41], v[178:179]
	v_pk_add_f32 v[42:43], v[38:39], v[176:177]
	v_pk_add_f32 v[48:49], v[36:37], v[182:183]
	v_pk_add_f32 v[46:47], v[34:35], v[180:181]
	s_cbranch_execz .LBB0_1378
	s_branch .LBB0_1381
.LBB0_1377:
.LBB0_1378:
	s_andn2_b64 vcc, exec, s[12:13]
	s_cbranch_vccnz .LBB0_1380
	s_waitcnt vmcnt(15)
	v_lshlrev_b32_e32 v46, 16, v196
	v_and_b32_e32 v47, 0xffff0000, v196
	v_lshlrev_b32_e32 v42, 16, v197
	v_and_b32_e32 v43, 0xffff0000, v197
	v_pk_add_f32 v[40:41], v[40:41], v[42:43]
	v_lshlrev_b32_e32 v42, 16, v198
	v_and_b32_e32 v43, 0xffff0000, v198
	v_lshlrev_b32_e32 v44, 16, v199
	v_and_b32_e32 v45, 0xffff0000, v199
	v_pk_add_f32 v[38:39], v[38:39], v[46:47]
	v_pk_add_f32 v[36:37], v[36:37], v[44:45]
	v_pk_add_f32 v[34:35], v[34:35], v[42:43]

; __device__ __forceinline__ unsigned cvt_pk_bf16(float lo, float hi) { unsigned r; asm volatile("v_cvt_pk_bf16_f32 %0, %1, %2" : "=v"(r) : "v"(lo), "v"(hi)); return r; }
;     __device__ __forceinline__ void operator()(const f32x4 (&acc)[2][2][4][2], const Unit& u, int wr, int wc, int fr, int fq) const {
;     ...
;             for (int m = 0; m < 4; ++m) { const size_t off = (size_t)(row0 + ai * HALF + m * 16) * ldc + col0; float sq_ = 0.f;
; #pragma unroll
;                 for (int bj = 0; bj < 2; ++bj) { f32x4 v0 = acc[ai][bj][m][0], v1 = acc[ai][bj][m][1];
;                     if (base32) { v0 += *(const f32x4*)(base32 + off + bj * HALF); v1 += *(const f32x4*)(base32 + off + bj * HALF + 4); }
;                     else if (base16) { const u32x4 b = *(const u32x4*)(base16 + off + bj * HALF);
;                         v0 += (f32x4){__uint_as_float(b.x << 16), __uint_as_float(b.x & 0xffff0000u), __uint_as_float(b.y << 16), __uint_as_float(b.y & 0xffff0000u)};
;                         v1 += (f32x4){__uint_as_float(b.z << 16), __uint_as_float(b.z & 0xffff0000u), __uint_as_float(b.w << 16), __uint_as_float(b.w & 0xffff0000u)}; }
;                     if (ssq) { float s_ = sq_; s_ = fmaf(v0[0], v0[0], s_); s_ = fmaf(v0[1], v0[1], s_); s_ = fmaf(v0[2], v0[2], s_); s_ = fmaf(v0[3], v0[3], s_);
;                       s_ = fmaf(v1[0], v1[0], s_); s_ = fmaf(v1[1], v1[1], s_); s_ = fmaf(v1[2], v1[2], s_); s_ = fmaf(v1[3], v1[3], s_); sq_ = s_; }
;                     u32x4 w; w.x = cvt_pk_bf16(v0[0], v0[1]); w.y = cvt_pk_bf16(v0[2], v0[3]); w.z = cvt_pk_bf16(v1[0], v1[1]); w.w = cvt_pk_bf16(v1[2], v1[3]);
;                     *(u32x4*)((u.kh ? out16b : out16) + off + bj * HALF) = w;
.LBB0_1381:
	v_cvt_pk_bf16_f32 v34, v42, v43
	v_cvt_pk_bf16_f32 v35, v44, v45
	v_cvt_pk_bf16_f32 v36, v46, v47
	v_cvt_pk_bf16_f32 v37, v48, v49
	global_store_dwordx4 v[50:51], v[34:37], off offset:256
	s_mov_b64 s[18:19], 0x50000
	s_and_b64 vcc, exec, s[42:43]
	v_lshlrev_b64 v[34:35], 11, v[138:139]
	v_lshl_add_u64 v[34:35], v[34:35], 0, v[140:141]
	v_lshl_add_u64 v[44:45], v[34:35], 0, s[18:19]
	v_lshl_add_u64 v[42:43], v[44:45], 2, s[14:15]
	s_cbranch_vccnz .LBB0_1383
	s_waitcnt vmcnt(10)
	v_pk_add_f32 v[36:37], v[32:33], v[186:187]
	v_pk_add_f32 v[34:35], v[30:31], v[184:185]
	v_pk_add_f32 v[40:41], v[28:29], v[190:191]
	v_pk_add_f32 v[38:39], v[26:27], v[188:189]
	s_cbranch_execz .LBB0_1384
	s_branch .LBB0_1387
.LBB0_1383:
.LBB0_1384:
	s_andn2_b64 vcc, exec, s[12:13]
	s_cbranch_vccnz .LBB0_1386
	s_waitcnt vmcnt(15)
	v_lshlrev_b32_e32 v38, 16, v208
	v_and_b32_e32 v39, 0xffff0000, v208
	v_lshlrev_b32_e32 v34, 16, v209
	v_and_b32_e32 v35, 0xffff0000, v209
	v_pk_add_f32 v[32:33], v[32:33], v[34:35]
	v_lshlrev_b32_e32 v34, 16, v210
	v_and_b32_e32 v35, 0xffff0000, v210
	v_lshlrev_b32_e32 v36, 16, v211
	v_and_b32_e32 v37, 0xffff0000, v211
	v_pk_add_f32 v[30:31], v[30:31], v[38:39]
	v_pk_add_f32 v[28:29], v[28:29], v[36:37]
	v_pk_add_f32 v[26:27], v[26:27], v[34:35]

; __device__ __forceinline__ unsigned cvt_pk_bf16(float lo, float hi) { unsigned r; asm volatile("v_cvt_pk_bf16_f32 %0, %1, %2" : "=v"(r) : "v"(lo), "v"(hi)); return r; }
;     __device__ __forceinline__ void operator()(const f32x4 (&acc)[2][2][4][2], const Unit& u, int wr, int wc, int fr, int fq) const {
;     ...
;             for (int m = 0; m < 4; ++m) { const size_t off = (size_t)(row0 + ai * HALF + m * 16) * ldc + col0; float sq_ = 0.f;
; #pragma unroll
;                 for (int bj = 0; bj < 2; ++bj) { f32x4 v0 = acc[ai][bj][m][0], v1 = acc[ai][bj][m][1];
;                     if (base32) { v0 += *(const f32x4*)(base32 + off + bj * HALF); v1 += *(const f32x4*)(base32 + off + bj * HALF + 4); }
;                     else if (base16) { const u32x4 b = *(const u32x4*)(base16 + off + bj * HALF);
;                         v0 += (f32x4){__uint_as_float(b.x << 16), __uint_as_float(b.x & 0xffff0000u), __uint_as_float(b.y << 16), __uint_as_float(b.y & 0xffff0000u)};
;                         v1 += (f32x4){__uint_as_float(b.z << 16), __uint_as_float(b.z & 0xffff0000u), __uint_as_float(b.w << 16), __uint_as_float(b.w & 0xffff0000u)}; }
;                     if (ssq) { float s_ = sq_; s_ = fmaf(v0[0], v0[0], s_); s_ = fmaf(v0[1], v0[1], s_); s_ = fmaf(v0[2], v0[2], s_); s_ = fmaf(v0[3], v0[3], s_);
;                       s_ = fmaf(v1[0], v1[0], s_); s_ = fmaf(v1[1], v1[1], s_); s_ = fmaf(v1[2], v1[2], s_); s_ = fmaf(v1[3], v1[3], s_); sq_ = s_; }
;                     u32x4 w; w.x = cvt_pk_bf16(v0[0], v0[1]); w.y = cvt_pk_bf16(v0[2], v0[3]); w.z = cvt_pk_bf16(v1[0], v1[1]); w.w = cvt_pk_bf16(v1[2], v1[3]);
;                     *(u32x4*)((u.kh ? out16b : out16) + off + bj * HALF) = w;
.LBB0_1387:
	v_cvt_pk_bf16_f32 v26, v34, v35
	v_lshl_add_u64 v[34:35], v[44:45], 1, s[0:1]
	s_and_b64 vcc, exec, s[42:43]
	v_cvt_pk_bf16_f32 v27, v36, v37
	v_cvt_pk_bf16_f32 v28, v38, v39
	v_cvt_pk_bf16_f32 v29, v40, v41
	global_store_dwordx4 v[34:35], v[26:29], off
	s_cbranch_vccnz .LBB0_1389
	s_waitcnt vmcnt(9)
	v_pk_add_f32 v[28:29], v[24:25], v[194:195]
	v_pk_add_f32 v[26:27], v[22:23], v[192:193]
	v_pk_add_f32 v[32:33], v[20:21], v[198:199]
	v_pk_add_f32 v[30:31], v[18:19], v[196:197]
	s_cbranch_execz .LBB0_1390
	s_branch .LBB0_1393
.LBB0_1389:
.LBB0_1390:
	s_andn2_b64 vcc, exec, s[12:13]
	s_cbranch_vccnz .LBB0_1392
	s_waitcnt vmcnt(15)
	v_lshlrev_b32_e32 v30, 16, v212
	v_and_b32_e32 v31, 0xffff0000, v212
	v_lshlrev_b32_e32 v26, 16, v213
	v_and_b32_e32 v27, 0xffff0000, v213
	v_pk_add_f32 v[24:25], v[24:25], v[26:27]
	v_lshlrev_b32_e32 v26, 16, v214
	v_and_b32_e32 v27, 0xffff0000, v214
	v_lshlrev_b32_e32 v28, 16, v215
	v_and_b32_e32 v29, 0xffff0000, v215
	v_pk_add_f32 v[22:23], v[22:23], v[30:31]
	v_pk_add_f32 v[20:21], v[20:21], v[28:29]
	v_pk_add_f32 v[18:19], v[18:19], v[26:27]

; __device__ __forceinline__ unsigned cvt_pk_bf16(float lo, float hi) { unsigned r; asm volatile("v_cvt_pk_bf16_f32 %0, %1, %2" : "=v"(r) : "v"(lo), "v"(hi)); return r; }
;     __device__ __forceinline__ void operator()(const f32x4 (&acc)[2][2][4][2], const Unit& u, int wr, int wc, int fr, int fq) const {
;     ...
;             for (int m = 0; m < 4; ++m) { const size_t off = (size_t)(row0 + ai * HALF + m * 16) * ldc + col0; float sq_ = 0.f;
; #pragma unroll
;                 for (int bj = 0; bj < 2; ++bj) { f32x4 v0 = acc[ai][bj][m][0], v1 = acc[ai][bj][m][1];
;                     if (base32) { v0 += *(const f32x4*)(base32 + off + bj * HALF); v1 += *(const f32x4*)(base32 + off + bj * HALF + 4); }
;                     else if (base16) { const u32x4 b = *(const u32x4*)(base16 + off + bj * HALF);
;                         v0 += (f32x4){__uint_as_float(b.x << 16), __uint_as_float(b.x & 0xffff0000u), __uint_as_float(b.y << 16), __uint_as_float(b.y & 0xffff0000u)};
;                         v1 += (f32x4){__uint_as_float(b.z << 16), __uint_as_float(b.z & 0xffff0000u), __uint_as_float(b.w << 16), __uint_as_float(b.w & 0xffff0000u)}; }
;                     if (ssq) { float s_ = sq_; s_ = fmaf(v0[0], v0[0], s_); s_ = fmaf(v0[1], v0[1], s_); s_ = fmaf(v0[2], v0[2], s_); s_ = fmaf(v0[3], v0[3], s_);
;                       s_ = fmaf(v1[0], v1[0], s_); s_ = fmaf(v1[1], v1[1], s_); s_ = fmaf(v1[2], v1[2], s_); s_ = fmaf(v1[3], v1[3], s_); sq_ = s_; }
;                     u32x4 w; w.x = cvt_pk_bf16(v0[0], v0[1]); w.y = cvt_pk_bf16(v0[2], v0[3]); w.z = cvt_pk_bf16(v1[0], v1[1]); w.w = cvt_pk_bf16(v1[2], v1[3]);
;                     *(u32x4*)((u.kh ? out16b : out16) + off + bj * HALF) = w;
.LBB0_1393:
	v_cvt_pk_bf16_f32 v18, v26, v27
	v_cvt_pk_bf16_f32 v19, v28, v29
	v_cvt_pk_bf16_f32 v20, v30, v31
	v_cvt_pk_bf16_f32 v21, v32, v33
	global_store_dwordx4 v[34:35], v[18:21], off offset:256
	s_mov_b64 s[18:19], 0x58000
	s_and_b64 vcc, exec, s[42:43]
	v_lshlrev_b64 v[18:19], 11, v[138:139]
	v_lshl_add_u64 v[18:19], v[18:19], 0, v[140:141]
	v_lshl_add_u64 v[28:29], v[18:19], 0, s[18:19]
	v_lshl_add_u64 v[26:27], v[28:29], 2, s[14:15]
	s_cbranch_vccnz .LBB0_1395
	s_waitcnt vmcnt(8)
	v_pk_add_f32 v[20:21], v[16:17], v[210:211]
	v_pk_add_f32 v[18:19], v[14:15], v[208:209]
	v_pk_add_f32 v[24:25], v[12:13], v[214:215]
	v_pk_add_f32 v[22:23], v[10:11], v[212:213]
	s_cbranch_execz .LBB0_1396
	s_branch .LBB0_1399
.LBB0_1395:
.LBB0_1396:
	s_andn2_b64 vcc, exec, s[12:13]
	s_cbranch_vccnz .LBB0_1398
	s_waitcnt vmcnt(15)
	v_lshlrev_b32_e32 v22, 16, v216
	v_and_b32_e32 v23, 0xffff0000, v216
	v_lshlrev_b32_e32 v18, 16, v217
	v_and_b32_e32 v19, 0xffff0000, v217
	v_pk_add_f32 v[16:17], v[16:17], v[18:19]
	v_lshlrev_b32_e32 v18, 16, v218
	v_and_b32_e32 v19, 0xffff0000, v218
	v_lshlrev_b32_e32 v20, 16, v219
	v_and_b32_e32 v21, 0xffff0000, v219
	v_pk_add_f32 v[14:15], v[14:15], v[22:23]
	v_pk_add_f32 v[12:13], v[12:13], v[20:21]
	v_pk_add_f32 v[10:11], v[10:11], v[18:19]

; __device__ __forceinline__ unsigned cvt_pk_bf16(float lo, float hi) { unsigned r; asm volatile("v_cvt_pk_bf16_f32 %0, %1, %2" : "=v"(r) : "v"(lo), "v"(hi)); return r; }
;     __device__ __forceinline__ void operator()(const f32x4 (&acc)[2][2][4][2], const Unit& u, int wr, int wc, int fr, int fq) const {
;     ...
;             for (int m = 0; m < 4; ++m) { const size_t off = (size_t)(row0 + ai * HALF + m * 16) * ldc + col0; float sq_ = 0.f;
; #pragma unroll
;                 for (int bj = 0; bj < 2; ++bj) { f32x4 v0 = acc[ai][bj][m][0], v1 = acc[ai][bj][m][1];
;                     if (base32) { v0 += *(const f32x4*)(base32 + off + bj * HALF); v1 += *(const f32x4*)(base32 + off + bj * HALF + 4); }
;                     else if (base16) { const u32x4 b = *(const u32x4*)(base16 + off + bj * HALF);
;                         v0 += (f32x4){__uint_as_float(b.x << 16), __uint_as_float(b.x & 0xffff0000u), __uint_as_float(b.y << 16), __uint_as_float(b.y & 0xffff0000u)};
;                         v1 += (f32x4){__uint_as_float(b.z << 16), __uint_as_float(b.z & 0xffff0000u), __uint_as_float(b.w << 16), __uint_as_float(b.w & 0xffff0000u)}; }
;                     if (ssq) { float s_ = sq_; s_ = fmaf(v0[0], v0[0], s_); s_ = fmaf(v0[1], v0[1], s_); s_ = fmaf(v0[2], v0[2], s_); s_ = fmaf(v0[3], v0[3], s_);
;                       s_ = fmaf(v1[0], v1[0], s_); s_ = fmaf(v1[1], v1[1], s_); s_ = fmaf(v1[2], v1[2], s_); s_ = fmaf(v1[3], v1[3], s_); sq_ = s_; }
;                     u32x4 w; w.x = cvt_pk_bf16(v0[0], v0[1]); w.y = cvt_pk_bf16(v0[2], v0[3]); w.z = cvt_pk_bf16(v1[0], v1[1]); w.w = cvt_pk_bf16(v1[2], v1[3]);
;                     *(u32x4*)((u.kh ? out16b : out16) + off + bj * HALF) = w;
.LBB0_1399:
	v_cvt_pk_bf16_f32 v10, v18, v19
	v_lshl_add_u64 v[18:19], v[28:29], 1, s[0:1]
	s_and_b64 vcc, exec, s[42:43]
	v_cvt_pk_bf16_f32 v11, v20, v21
	v_cvt_pk_bf16_f32 v12, v22, v23
	v_cvt_pk_bf16_f32 v13, v24, v25
	global_store_dwordx4 v[18:19], v[10:13], off
	s_cbranch_vccnz .LBB0_1401
	s_waitcnt vmcnt(7)
	v_pk_add_f32 v[12:13], v[8:9], v[218:219]
	v_pk_add_f32 v[10:11], v[6:7], v[216:217]
	v_pk_add_f32 v[16:17], v[4:5], v[222:223]
	v_pk_add_f32 v[14:15], v[2:3], v[220:221]
	s_cbranch_execz .LBB0_1402
	s_branch .LBB0_1405
.LBB0_1401:
.LBB0_1402:
	s_andn2_b64 vcc, exec, s[12:13]
	s_cbranch_vccnz .LBB0_1404
	s_waitcnt vmcnt(15)
	v_lshlrev_b32_e32 v14, 16, v220
	v_and_b32_e32 v15, 0xffff0000, v220
	v_lshlrev_b32_e32 v10, 16, v221
	v_and_b32_e32 v11, 0xffff0000, v221
	v_pk_add_f32 v[8:9], v[8:9], v[10:11]
	v_lshlrev_b32_e32 v10, 16, v222
	v_and_b32_e32 v11, 0xffff0000, v222
	v_lshlrev_b32_e32 v12, 16, v223
	v_and_b32_e32 v13, 0xffff0000, v223
	v_pk_add_f32 v[6:7], v[6:7], v[14:15]
	v_pk_add_f32 v[4:5], v[4:5], v[12:13]
	v_pk_add_f32 v[2:3], v[2:3], v[10:11]

; #define LAS __attribute__((address_space(3)))
; #define LDS_WAIT() asm volatile("s_waitcnt lgkmcnt(0)" ::: "memory")
; #define tid (tid_of(wave))
; __device__ __forceinline__ void build_tile_table(const Ptrs& P, bool moe, volatile LAS unsigned* MISC, int tid) {
;     if (tid == 0) { unsigned t = 0u; MISC[16] = 0u;
;         for (int e = 0; e < 8; ++e) { const unsigned cnt = moe ? __hip_atomic_load(P.ctl + CW_CNT + 64 * e, RLX_AGENT) : (e == 0 ? (unsigned)M : 0u); t += (cnt + 255u) >> 8; if (t > (unsigned)(MPAD / 256)) t = MPAD / 256; MISC[17 + e] = t; } }
;     LDS_WAIT(); __syncthreads();
; }
.LBB0_1610:
	s_andn2_b64 vcc, exec, s[0:1]
	s_cbranch_vccnz .LBB0_1684
	s_mov_b32 s16, s90
	s_ashr_i32 s17, s16, 31
	v_readlane_b32 s0, v251, 3
	v_mbcnt_lo_u32_b32 v0, -1, 0
	v_mbcnt_hi_u32_b32 v0, -1, v0
	s_add_u32 s0, s0, s16
	v_readlane_b32 s1, v251, 4
	v_add_u32_e32 v0, s94, v0
	s_addc_u32 s1, s1, s17
	s_nop 0
	v_cmp_eq_u32_e32 vcc, 0, v0
	s_and_saveexec_b64 s[14:15], vcc
	s_cbranch_execz .LBB0_1613
	v_readlane_b32 s18, v254, 8
	s_waitcnt vmcnt(0) lgkmcnt(0)
	v_mov_b32_e32 v3, 0x8000
	v_mov_b32_e32 v0, s18
	ds_write_b32 v0, v1
	v_mov_b32_e32 v11, 0x8000
	global_load_dword v4, v11, s[0:1] offset:1280 sc1
	global_load_dword v5, v11, s[0:1] offset:1536 sc1
	global_load_dword v6, v11, s[0:1] offset:1792 sc1
	global_load_dword v7, v11, s[0:1] offset:2048 sc1
	global_load_dword v8, v11, s[0:1] offset:2304 sc1
	global_load_dword v9, v11, s[0:1] offset:2560 sc1
	global_load_dword v10, v11, s[0:1] offset:2816 sc1
	global_load_dword v0, v3, s[0:1] offset:1024 sc1
	v_readlane_b32 s18, v254, 9
	s_waitcnt vmcnt(0)
	v_add_u32_e32 v0, 0xff, v0
	v_lshrrev_b32_e32 v0, 8, v0
	v_min_u32_e32 v0, 0x48, v0
	v_mov_b32_e32 v2, s18
	ds_write_b32 v2, v0
	v_mov_b32_e32 v2, v4
	v_readlane_b32 s18, v254, 10
	s_waitcnt vmcnt(0)
	v_add_u32_e32 v2, 0xff, v2
	v_lshrrev_b32_e32 v2, 8, v2
	v_add_u32_e32 v0, v2, v0
	v_min_u32_e32 v0, 0x48, v0
	v_mov_b32_e32 v2, s18
	ds_write_b32 v2, v0
	v_mov_b32_e32 v2, v5
	v_readlane_b32 s18, v254, 11
	s_waitcnt vmcnt(0)
	v_add_u32_e32 v2, 0xff, v2
	v_lshrrev_b32_e32 v2, 8, v2
	v_add_u32_e32 v0, v2, v0
	v_min_u32_e32 v0, 0x48, v0
	v_mov_b32_e32 v2, s18
	ds_write_b32 v2, v0
	v_mov_b32_e32 v2, v6
	v_readlane_b32 s18, v254, 12
	s_waitcnt vmcnt(0)
	v_add_u32_e32 v2, 0xff, v2
	v_lshrrev_b32_e32 v2, 8, v2
	v_add_u32_e32 v0, v2, v0
	v_min_u32_e32 v0, 0x48, v0
	v_mov_b32_e32 v2, s18
	ds_write_b32 v2, v0
	v_mov_b32_e32 v2, v7
	v_readlane_b32 s18, v254, 13
	s_waitcnt vmcnt(0)
	v_add_u32_e32 v2, 0xff, v2
	v_lshrrev_b32_e32 v2, 8, v2
	v_add_u32_e32 v0, v2, v0
	v_min_u32_e32 v0, 0x48, v0
	v_mov_b32_e32 v2, s18
	ds_write_b32 v2, v0
	v_mov_b32_e32 v2, v8
	v_readlane_b32 s18, v254, 14
	s_waitcnt vmcnt(0)
	v_add_u32_e32 v2, 0xff, v2
	v_lshrrev_b32_e32 v2, 8, v2
	v_add_u32_e32 v0, v2, v0
	v_min_u32_e32 v0, 0x48, v0
	v_mov_b32_e32 v2, s18
	ds_write_b32 v2, v0
	v_mov_b32_e32 v2, v9
	v_readlane_b32 s18, v254, 15
	s_waitcnt vmcnt(0)
	v_add_u32_e32 v2, 0xff, v2
	v_lshrrev_b32_e32 v2, 8, v2
	v_add_u32_e32 v0, v2, v0
	v_min_u32_e32 v0, 0x48, v0
	v_mov_b32_e32 v2, s18
	ds_write_b32 v2, v0
	v_mov_b32_e32 v2, v10
	v_readlane_b32 s18, v254, 16
	s_waitcnt vmcnt(0)
	v_add_u32_e32 v2, 0xff, v2
	v_lshrrev_b32_e32 v2, 8, v2
	v_add_u32_e32 v0, v2, v0
	v_min_u32_e32 v0, 0x48, v0
	v_mov_b32_e32 v2, s18
	ds_write_b32 v2, v0

; #define LAS __attribute__((address_space(3)))
; #define LDS_WAIT() asm volatile("s_waitcnt lgkmcnt(0)" ::: "memory")
; #define tid (tid_of(wave))
; __device__ __forceinline__ void build_tile_table(const Ptrs& P, bool moe, volatile LAS unsigned* MISC, int tid) {
;     if (tid == 0) { unsigned t = 0u; MISC[16] = 0u;
;         for (int e = 0; e < 8; ++e) { const unsigned cnt = moe ? __hip_atomic_load(P.ctl + CW_CNT + 64 * e, RLX_AGENT) : (e == 0 ? (unsigned)M : 0u); t += (cnt + 255u) >> 8; if (t > (unsigned)(MPAD / 256)) t = MPAD / 256; MISC[17 + e] = t; } }
;     LDS_WAIT(); __syncthreads();
; }
; __global__ void __launch_bounds__(NWAVES * 64, 2) hybrid_fwd(Args args) {
;     ...
;         if (PH(PB + 8)) {
;             const Ptrs P = make_ptrs(args, ws0);
;             build_tile_table(P, layer == 1, MISC, tid);
;             pg8::GroupSched S; S.nMt = __builtin_amdgcn_readfirstlane((int)MISC[24]); S.nN = NGU / 256; S.nwg = S.nMt * S.nN;
.LBB0_1686:
	s_andn2_b64 vcc, exec, s[0:1]
	s_cbranch_vccnz .LBB0_1913
	s_mov_b32 s0, s90
	s_ashr_i32 s1, s0, 31
	s_lshl_b64 s[14:15], s[0:1], 3
	s_add_u32 s14, s88, s14
	s_addc_u32 s15, s89, s15
	v_readlane_b32 s16, v251, 3
	s_add_u32 s0, s16, s0
	v_readlane_b32 s16, v251, 4
	s_addc_u32 s1, s16, s1
	s_load_dwordx4 s[68:71], s[14:15], 0x8
	s_load_dwordx2 s[16:17], s[14:15], 0x30
	s_load_dwordx4 s[64:67], s[14:15], 0x40
	s_load_dwordx2 s[4:5], s[14:15], 0x50
	s_load_dwordx2 s[22:23], s[14:15], 0x70
	s_load_dwordx4 s[24:27], s[14:15], 0x60
	v_mbcnt_lo_u32_b32 v0, -1, 0
	v_mbcnt_hi_u32_b32 v0, -1, v0
	s_nop 0
	v_add_u32_e32 v0, s94, v0
	s_nop 0
	v_cmp_eq_u32_e32 vcc, 0, v0
	s_and_saveexec_b64 s[14:15], vcc
	s_cbranch_execz .LBB0_1705
	v_readlane_b32 s18, v254, 8
	s_waitcnt vmcnt(0)
	v_mov_b32_e32 v2, 32
	v_mov_b32_e32 v0, s18
	v_readlane_b32 s18, v254, 22
	v_readlane_b32 s19, v254, 23
	ds_write_b32 v0, v1
	s_andn2_b64 vcc, exec, s[18:19]
	v_cndmask_b32_e64 v0, 0, 1, s[18:19]
	v_cmp_ne_u32_e64 s[38:39], 1, v0
	s_cbranch_vccnz .LBB0_1690
	v_mov_b32_e32 v11, 0x8000
	global_load_dword v4, v11, s[0:1] offset:1280 sc1
	global_load_dword v5, v11, s[0:1] offset:1536 sc1
	global_load_dword v6, v11, s[0:1] offset:1792 sc1
	global_load_dword v7, v11, s[0:1] offset:2048 sc1
	global_load_dword v8, v11, s[0:1] offset:2304 sc1
	global_load_dword v9, v11, s[0:1] offset:2560 sc1
	global_load_dword v10, v11, s[0:1] offset:2816 sc1
	v_mov_b32_e32 v0, 0x8000
	global_load_dword v0, v0, s[0:1] offset:1024 sc1
	s_waitcnt vmcnt(0)
	v_add_u32_e32 v0, 0xff, v0
	v_lshrrev_b32_e32 v0, 8, v0
	v_min_u32_e32 v2, 0x48, v0
.LBB0_1690:
	v_readlane_b32 s18, v254, 9
	s_and_b64 vcc, exec, s[38:39]
	s_waitcnt lgkmcnt(0)
	v_mov_b32_e32 v3, 0
	v_mov_b32_e32 v0, s18
	ds_write_b32 v0, v2
	v_mov_b32_e32 v0, 0
	s_cbranch_vccnz .LBB0_1692
	v_mov_b32_e32 v3, v4
	v_add_u32_e32 v3, 0xff, v3
	v_lshrrev_b32_e32 v3, 8, v3
.LBB0_1692:
	v_add_u32_e32 v2, v3, v2
	v_readlane_b32 s18, v254, 10
	v_min_u32_e32 v2, 0x48, v2
	s_and_b64 vcc, exec, s[38:39]
	v_mov_b32_e32 v3, s18
	ds_write_b32 v3, v2
	s_cbranch_vccnz .LBB0_1694
	v_mov_b32_e32 v0, v5
	v_add_u32_e32 v0, 0xff, v0
	v_lshrrev_b32_e32 v0, 8, v0
.LBB0_1694:
	v_add_u32_e32 v0, v0, v2
	v_readlane_b32 s18, v254, 11
	v_min_u32_e32 v2, 0x48, v0
	s_and_b64 vcc, exec, s[38:39]
	v_mov_b32_e32 v0, s18
	ds_write_b32 v0, v2
	v_mov_b32_e32 v0, 0
	v_mov_b32_e32 v3, 0
	s_cbranch_vccnz .LBB0_1696
	v_mov_b32_e32 v3, v6
	v_add_u32_e32 v3, 0xff, v3
	v_lshrrev_b32_e32 v3, 8, v3
.LBB0_1696:
	v_add_u32_e32 v2, v3, v2
	v_readlane_b32 s18, v254, 12
	v_min_u32_e32 v2, 0x48, v2
	s_and_b64 vcc, exec, s[38:39]
	v_mov_b32_e32 v3, s18
	ds_write_b32 v3, v2
	s_cbranch_vccnz .LBB0_1698
	v_mov_b32_e32 v0, v7
	v_add_u32_e32 v0, 0xff, v0
	v_lshrrev_b32_e32 v0, 8, v0
.LBB0_1698:
	v_add_u32_e32 v0, v0, v2
	v_readlane_b32 s18, v254, 13
	v_min_u32_e32 v2, 0x48, v0
	s_and_b64 vcc, exec, s[38:39]
	v_mov_b32_e32 v0, s18
	ds_write_b32 v0, v2
	v_mov_b32_e32 v0, 0
	v_mov_b32_e32 v3, 0
	s_cbranch_vccnz .LBB0_1700
	v_mov_b32_e32 v3, v8
	v_add_u32_e32 v3, 0xff, v3
	v_lshrrev_b32_e32 v3, 8, v3
.LBB0_1700:
	v_add_u32_e32 v2, v3, v2
	v_readlane_b32 s18, v254, 14
	v_min_u32_e32 v2, 0x48, v2
	s_and_b64 vcc, exec, s[38:39]
	v_mov_b32_e32 v3, s18
	ds_write_b32 v3, v2
	s_cbranch_vccnz .LBB0_1702
	v_mov_b32_e32 v0, v9
	v_add_u32_e32 v0, 0xff, v0
	v_lshrrev_b32_e32 v0, 8, v0
.LBB0_1702:
	v_add_u32_e32 v0, v0, v2
	v_readlane_b32 s18, v254, 15
	v_min_u32_e32 v0, 0x48, v0
	s_and_b64 vcc, exec, s[38:39]
	v_mov_b32_e32 v2, s18
	ds_write_b32 v2, v0
	v_mov_b32_e32 v2, 0
	s_cbranch_vccnz .LBB0_1704
	v_mov_b32_e32 v2, v10
	v_add_u32_e32 v2, 0xff, v2
	v_lshrrev_b32_e32 v2, 8, v2

; #define LAS __attribute__((address_space(3)))
; #define LDS_WAIT() asm volatile("s_waitcnt lgkmcnt(0)" ::: "memory")
; #define tid (tid_of(wave))
; __device__ __forceinline__ void build_tile_table(const Ptrs& P, bool moe, volatile LAS unsigned* MISC, int tid) {
;     if (tid == 0) { unsigned t = 0u; MISC[16] = 0u;
;         for (int e = 0; e < 8; ++e) { const unsigned cnt = moe ? __hip_atomic_load(P.ctl + CW_CNT + 64 * e, RLX_AGENT) : (e == 0 ? (unsigned)M : 0u); t += (cnt + 255u) >> 8; if (t > (unsigned)(MPAD / 256)) t = MPAD / 256; MISC[17 + e] = t; } }
;     LDS_WAIT(); __syncthreads();
; }
; __global__ void __launch_bounds__(NWAVES * 64, 2) hybrid_fwd(Args args) {
;     ...
;         if (PH(PB + 9)) {
;             const Ptrs P = make_ptrs(args, ws0);
;             build_tile_table(P, layer == 1, MISC, tid);
.LBB0_1913:
	s_cmp_le_i32 s76, s38
	s_cselect_b64 s[0:1], -1, 0
	s_cmp_lt_i32 s38, s77
	s_cselect_b64 s[14:15], -1, 0
	s_and_b64 s[0:1], s[0:1], s[14:15]
	s_andn2_b64 vcc, exec, s[0:1]
	s_movk_i32 s38, 0x1000
	s_cbranch_vccnz .LBB0_2095
	s_mov_b32 s14, s90
	s_ashr_i32 s15, s14, 31
	v_readlane_b32 s16, v251, 3
	v_mbcnt_lo_u32_b32 v0, -1, 0
	v_mbcnt_hi_u32_b32 v0, -1, v0
	s_add_u32 s22, s16, s14
	v_readlane_b32 s14, v251, 4
	v_add_u32_e32 v0, s94, v0
	s_addc_u32 s23, s14, s15
	s_nop 0
	v_cmp_eq_u32_e32 vcc, 0, v0
	s_and_saveexec_b64 s[14:15], vcc
	s_cbranch_execz .LBB0_1932
	v_readlane_b32 s16, v254, 8
	s_waitcnt vmcnt(0)
	v_mov_b32_e32 v2, 32
	v_mov_b32_e32 v0, s16
	v_readlane_b32 s16, v254, 22
	v_readlane_b32 s17, v254, 23
	ds_write_b32 v0, v1
	s_andn2_b64 vcc, exec, s[16:17]
	v_cndmask_b32_e64 v0, 0, 1, s[16:17]
	v_cmp_ne_u32_e64 s[38:39], 1, v0
	s_cbranch_vccnz .LBB0_1917
	v_mov_b32_e32 v11, 0x8000
	global_load_dword v4, v11, s[22:23] offset:1280 sc1
	global_load_dword v5, v11, s[22:23] offset:1536 sc1
	global_load_dword v6, v11, s[22:23] offset:1792 sc1
	global_load_dword v7, v11, s[22:23] offset:2048 sc1
	global_load_dword v8, v11, s[22:23] offset:2304 sc1
	global_load_dword v9, v11, s[22:23] offset:2560 sc1
	global_load_dword v10, v11, s[22:23] offset:2816 sc1
	v_mov_b32_e32 v0, 0x8000
	global_load_dword v0, v0, s[22:23] offset:1024 sc1
	s_waitcnt vmcnt(0)
	v_add_u32_e32 v0, 0xff, v0
	v_lshrrev_b32_e32 v0, 8, v0
	v_min_u32_e32 v2, 0x48, v0
.LBB0_1917:
	v_readlane_b32 s16, v254, 9
	s_and_b64 vcc, exec, s[38:39]
	s_waitcnt lgkmcnt(0)
	v_mov_b32_e32 v3, 0
	v_mov_b32_e32 v0, s16
	ds_write_b32 v0, v2
	v_mov_b32_e32 v0, 0
	s_cbranch_vccnz .LBB0_1919
	v_mov_b32_e32 v3, v4
	v_add_u32_e32 v3, 0xff, v3
	v_lshrrev_b32_e32 v3, 8, v3
.LBB0_1919:
	v_add_u32_e32 v2, v3, v2
	v_readlane_b32 s16, v254, 10
	v_min_u32_e32 v2, 0x48, v2
	s_and_b64 vcc, exec, s[38:39]
	v_mov_b32_e32 v3, s16
	ds_write_b32 v3, v2
	s_cbranch_vccnz .LBB0_1921
	v_mov_b32_e32 v0, v5
	v_add_u32_e32 v0, 0xff, v0
	v_lshrrev_b32_e32 v0, 8, v0
.LBB0_1921:
	v_add_u32_e32 v0, v0, v2
	v_readlane_b32 s16, v254, 11
	v_min_u32_e32 v2, 0x48, v0
	s_and_b64 vcc, exec, s[38:39]
	v_mov_b32_e32 v0, s16
	ds_write_b32 v0, v2
	v_mov_b32_e32 v0, 0
	v_mov_b32_e32 v3, 0
	s_cbranch_vccnz .LBB0_1923
	v_mov_b32_e32 v3, v6
	v_add_u32_e32 v3, 0xff, v3
	v_lshrrev_b32_e32 v3, 8, v3
.LBB0_1923:
	v_add_u32_e32 v2, v3, v2
	v_readlane_b32 s16, v254, 12
	v_min_u32_e32 v2, 0x48, v2
	s_and_b64 vcc, exec, s[38:39]
	v_mov_b32_e32 v3, s16
	ds_write_b32 v3, v2
	s_cbranch_vccnz .LBB0_1925
	v_mov_b32_e32 v0, v7
	v_add_u32_e32 v0, 0xff, v0
	v_lshrrev_b32_e32 v0, 8, v0
.LBB0_1925:
	v_add_u32_e32 v0, v0, v2
	v_readlane_b32 s16, v254, 13
	v_min_u32_e32 v2, 0x48, v0
	s_and_b64 vcc, exec, s[38:39]
	v_mov_b32_e32 v0, s16
	ds_write_b32 v0, v2
	v_mov_b32_e32 v0, 0
	v_mov_b32_e32 v3, 0
	s_cbranch_vccnz .LBB0_1927
	v_mov_b32_e32 v3, v8
	v_add_u32_e32 v3, 0xff, v3
	v_lshrrev_b32_e32 v3, 8, v3
.LBB0_1927:
	v_add_u32_e32 v2, v3, v2
	v_readlane_b32 s16, v254, 14
	v_min_u32_e32 v2, 0x48, v2
	s_and_b64 vcc, exec, s[38:39]
	v_mov_b32_e32 v3, s16
	ds_write_b32 v3, v2
	s_cbranch_vccnz .LBB0_1929
	v_mov_b32_e32 v0, v9
	v_add_u32_e32 v0, 0xff, v0
	v_lshrrev_b32_e32 v0, 8, v0
.LBB0_1929:
	v_add_u32_e32 v0, v0, v2
	v_readlane_b32 s16, v254, 15
	v_min_u32_e32 v0, 0x48, v0
	s_and_b64 vcc, exec, s[38:39]
	v_mov_b32_e32 v2, s16
	ds_write_b32 v2, v0
	v_mov_b32_e32 v2, 0
	s_cbranch_vccnz .LBB0_1931
	v_mov_b32_e32 v2, v10
	v_add_u32_e32 v2, 0xff, v2
	v_lshrrev_b32_e32 v2, 8, v2
